# conv-in-NSA: per-iteration convert/store/load block moved from the loop latch to the start of the softmax segment (slack against the other wave group's PV+QK), decode uses 3 scalar temps
# speedup vs baseline: 1.0520x; 1.0150x over previous
; __device__ __forceinline__ void p0_weights(const Args& a, LAS unsigned char* lds) {
;     ...
;         else if ((r -= I_FD) < 16 * I_MG) { const int up = r / (8 * I_MG); r -= up * 8 * I_MG; const int e = r / I_MG; r -= e * I_MG; W = a.in[up ? I_MWU : I_MWG] + (size_t)e * D * DFE; w.K = D; w.N = DFE;
;             w.dst = a.ws + WS_MGU_T + (size_t)e * 2 * DFE * D * (MOE_FP8 ? 1 : 2); w.kind = 2 + up; w.f8 = MOE_FP8; w.scale = F8_WGU; }
;         else { r -= 16 * I_MG; const int e = r / I_MD; r -= e * I_MD; W = a.in[I_MWD] + (size_t)e * DFE * D; w.K = DFE; w.N = D; w.dst = a.ws + WS_MD_T + (size_t)e * D * DFE * (MOE_FP8 ? 1 : 2); w.f8 = MOE_FP8; w.scale = F8_WD; }
;         const int nblk = (w.N + 31) >> 5, kb = r / nblk, nb = r - kb * nblk;
;         w.k0 = 128 * kb + 16 * (lane >> 3); w.n = 32 * nb + 4 * (lane & 7); w.valid = w.n < w.N; w.src = W + (size_t)w.k0 * w.N + w.n;
; __device__ __forceinline__ void nsa_unit(const Args& a, LAS unsigned char* lds, int b, int kvh, int qb) {
;     ...
; #pragma unroll
;     for (int dt = 0; dt < 4; ++dt)
; #pragma unroll
;         for (int i = 0; i < 16; ++i) o[dt][i] = 0.f;
;     float mrun = -1e30f, lrun = 0.f;
;     f32x16 p0, p1;
; #pragma unroll
;     for (int i = 0; i < 16; ++i) { p0[i] = 0.f; p1[i] = 0.f; }
;     bf16x8 pf[2][2];
;     if (w >= 4) asm volatile("s_barrier" ::: "memory");
.LBB0_894:
	s_cmp_lt_i32 s15, -1
	s_cbranch_scc1 .LBB0_919
	v_mov_b32_e32 v49, v47
	s_lshl_b32 s0, s72, 1
	s_max_i32 s1, s72, 8
	v_mov_b32_e32 v60, v47
	v_mov_b32_e32 v61, v47
	v_lshl_add_u64 v[206:207], s[30:31], 0, v[48:49]
	s_sub_i32 s63, s0, s1
	v_mov_b32_e32 v46, v47
	v_mov_b32_e32 v48, v47
	v_mov_b32_e32 v50, v47
	v_mov_b32_e32 v51, v47
	v_mov_b32_e32 v52, v47
	v_mov_b32_e32 v53, v47
	v_mov_b32_e32 v54, v47
	v_mov_b32_e32 v55, v47
	v_mov_b32_e32 v56, v47
	v_mov_b32_e32 v57, v47
	v_mov_b32_e32 v58, v47
	v_mov_b32_e32 v59, v47
	v_mov_b64_e32 v[108:109], v[60:61]
	v_mov_b64_e32 v[124:125], v[60:61]
	v_mov_b64_e32 v[140:141], v[60:61]
	v_mov_b64_e32 v[156:157], v[60:61]
	v_mov_b64_e32 v[76:77], v[60:61]
	v_mov_b64_e32 v[92:93], v[60:61]
	v_add_u32_e32 v43, 1, v249
	s_add_i32 s23, s63, 11
	s_add_i32 s24, s63, 10
	s_mov_b32 s62, 2
	s_add_i32 s63, s63, 2
	s_mov_b32 s74, 0
	v_mov_b32_e32 v208, 0xf149f2ca
	v_mov_b32_e32 v209, 0
	s_movk_i32 s75, 0xc000
	v_mov_b64_e32 v[106:107], v[58:59]
	v_mov_b64_e32 v[104:105], v[56:57]
	v_mov_b64_e32 v[102:103], v[54:55]
	v_mov_b64_e32 v[100:101], v[52:53]
	v_mov_b64_e32 v[98:99], v[50:51]
	v_mov_b64_e32 v[96:97], v[48:49]
	v_mov_b64_e32 v[94:95], v[46:47]
	v_mov_b64_e32 v[122:123], v[58:59]
	v_mov_b64_e32 v[120:121], v[56:57]
	v_mov_b64_e32 v[118:119], v[54:55]
	v_mov_b64_e32 v[116:117], v[52:53]
	v_mov_b64_e32 v[114:115], v[50:51]
	v_mov_b64_e32 v[112:113], v[48:49]
	v_mov_b64_e32 v[110:111], v[46:47]
	v_mov_b64_e32 v[138:139], v[58:59]
	v_mov_b64_e32 v[136:137], v[56:57]
	v_mov_b64_e32 v[134:135], v[54:55]
	v_mov_b64_e32 v[132:133], v[52:53]
	v_mov_b64_e32 v[130:131], v[50:51]
	v_mov_b64_e32 v[128:129], v[48:49]
	v_mov_b64_e32 v[126:127], v[46:47]
	v_mov_b64_e32 v[154:155], v[58:59]
	v_mov_b64_e32 v[152:153], v[56:57]
	v_mov_b64_e32 v[150:151], v[54:55]
	v_mov_b64_e32 v[148:149], v[52:53]
	v_mov_b64_e32 v[146:147], v[50:51]
	v_mov_b64_e32 v[144:145], v[48:49]
	v_mov_b64_e32 v[142:143], v[46:47]
	v_mov_b64_e32 v[74:75], v[58:59]
	v_mov_b64_e32 v[72:73], v[56:57]
	v_mov_b64_e32 v[70:71], v[54:55]
	v_mov_b64_e32 v[68:69], v[52:53]
	v_mov_b64_e32 v[66:67], v[50:51]
	v_mov_b64_e32 v[64:65], v[48:49]
	v_mov_b64_e32 v[62:63], v[46:47]
	v_mov_b64_e32 v[90:91], v[58:59]
	v_mov_b64_e32 v[88:89], v[56:57]
	v_mov_b64_e32 v[86:87], v[54:55]
	v_mov_b64_e32 v[84:85], v[52:53]
	v_mov_b64_e32 v[82:83], v[50:51]
	v_mov_b64_e32 v[80:81], v[48:49]
	v_mov_b64_e32 v[78:79], v[46:47]
	s_mov_b32 s67, 0
	s_and_b32 s12, s101, 3
	s_lshl_b32 s12, s12, 28
	s_andn2_b32 s101, s101, 0x30000000
	s_or_b32 s101, s101, s12
	s_and_b32 s12, s101, 0xfffffff
	s_cmp_ge_u32 s12, 168
	s_cbranch_scc1 .Lcn_ldum_n0s
	s_and_b32 s12, s101, 0xfffffff
	s_lshr_b32 s13, s12, 2
	s_lshl_b32 s13, s13, 11
	s_add_u32 s13, s13, s100
	s_lshr_b32 s65, s13, 9
	s_mul_i32 s65, s65, 0x2493
	s_lshr_b32 s65, s65, 16
	s_mul_i32 s32, s65, 0xe00
	s_sub_u32 s13, s13, s32
	s_and_b32 s12, s12, 3
	s_cmp_ge_u32 s65, 16
	s_cbranch_scc1 .Lcn_dn_n0ss
	s_lshr_b32 s32, s13, 5
	s_mul_i32 s32, s32, 0x2493
	s_lshr_b32 s32, s32, 16
	s_mul_i32 s33, s32, 0xe0
	s_sub_u32 s33, s13, s33
	s_lshl_b32 s32, s32, 2
	s_add_u32 s32, s32, s12
	s_lshr_b32 s13, s65, 1
	s_and_b32 s65, s65, 1
	s_mul_i32 s12, s13, 0x3800000
	s_mul_i32 s13, s32, 0xe0000
	s_add_u32 s12, s12, s13
	s_lshl_b32 s13, s33, 7
	s_add_u32 s12, s12, s13
	v_readlane_b32 s32, v255, 46
	v_readlane_b32 s33, v255, 47
	s_cmp_eq_u32 s65, 0
	s_cselect_b32 s32, s98, s32
	s_cselect_b32 s33, s99, s33
	s_add_u32 s32, s32, s12
	s_addc_u32 s33, s33, 0
	s_movk_i32 s65, 0x7000
	s_branch .Lcn_dd_n0ss
.Lcn_dn_n0ss:
	s_lshr_b32 s32, s13, 6
	s_and_b32 s33, s13, 63
	s_lshl_b32 s32, s32, 2
	s_add_u32 s32, s32, s12
	s_sub_u32 s13, s65, 16
	s_mul_i32 s12, s13, 0x3800000
	s_lshl_b32 s13, s32, 18
	s_add_u32 s12, s12, s13
	s_lshl_b32 s13, s33, 7
	s_add_u32 s12, s12, s13
	v_readlane_b32 s32, v255, 48
	v_readlane_b32 s33, v255, 49
	s_add_u32 s32, s32, s12
	s_addc_u32 s33, s33, 0
	s_movk_i32 s65, 0x2000

; __device__ __forceinline__ void witem_load(const WItem& w, f32x4 (&v)[16]) {
;     if (!w.valid) return;
; #pragma unroll
;     for (int i = 0; i < 16; ++i) v[i] = *(const f32x4*)(w.src + (size_t)i * w.N);
; }
.Lcn_ldum_n0s:
	v_readlane_b32 s32, v255, 52
	v_readlane_b32 s33, v255, 53
	s_add_u32 s32, s32, 0x500000
	s_addc_u32 s33, s33, 0
	s_movk_i32 s65, 0x2000
	s_mov_b32 s25, 0
.Lcn_lgo_n0s:
	v_and_b32_e32 v224, 63, v0
	v_and_b32_e32 v253, 7, v224
	v_lshrrev_b32_e32 v224, 3, v224
	v_lshlrev_b32_e32 v224, 2, v224
	v_lshlrev_b32_e32 v225, 4, v253
	v_lshlrev_b32_e32 v253, 2, v253
	v_mad_u32_u24 v254, v224, s65, v225
	global_load_dwordx4 v[212:215], v254, s[32:33] nt
	s_add_u32 s32, s32, s65
	s_addc_u32 s33, s33, 0
	global_load_dwordx4 v[216:219], v254, s[32:33] nt
	s_add_u32 s32, s32, s65
	s_addc_u32 s33, s33, 0
	global_load_dwordx4 v[220:223], v254, s[32:33] nt
	s_add_u32 s32, s32, s65
	s_addc_u32 s33, s33, 0
	global_load_dwordx2 v[224:225], v254, s[32:33] offset:0 nt
	global_load_dword v253, v254, s[32:33] offset:8 nt
	global_load_dword v254, v254, s[32:33] offset:12 nt
	s_branch .LBB0_897

; __device__ __forceinline__ void nsa_unit(const Args& a, LAS unsigned char* lds, int b, int kvh, int qb) {
;     ...
;         if (it + 1 < nTot) asm volatile("s_waitcnt vmcnt(4) lgkmcnt(0)\n\ts_barrier" ::: "memory"); else asm volatile("s_waitcnt vmcnt(0) lgkmcnt(0)\n\ts_barrier" ::: "memory");
;         if (it > 0) { const int ti = it - 1;
.LBB0_902:
	s_add_i32 s12, s74, 1
	s_cmp_gt_i32 s12, s15
	s_cbranch_scc1 .Lcn_w0_n0
	s_waitcnt vmcnt(4)
	s_branch .Lcn_wd_n0

; __device__ __forceinline__ unsigned pk4_fp8(float a, float b, float c, float d) { int p = __builtin_amdgcn_cvt_pk_fp8_f32(a, b, 0, false); p = __builtin_amdgcn_cvt_pk_fp8_f32(c, d, p, true); return (unsigned)p; }
; __device__ __forceinline__ void witem_store(const WItem& w, const f32x4 (&v)[16]) {
;     if (!w.valid) return;
;     if (w.f8) {
; #pragma unroll
;         for (int j = 0; j < 4; ++j) { u32x4 o; const float sc = w.scale;
;             o.x = pk4_fp8(v[0][j] * sc, v[1][j] * sc, v[2][j] * sc, v[3][j] * sc); o.y = pk4_fp8(v[4][j] * sc, v[5][j] * sc, v[6][j] * sc, v[7][j] * sc);
;             o.z = pk4_fp8(v[8][j] * sc, v[9][j] * sc, v[10][j] * sc, v[11][j] * sc); o.w = pk4_fp8(v[12][j] * sc, v[13][j] * sc, v[14][j] * sc, v[15][j] * sc);
;             *(u32x4*)(w.dst + (size_t)witem_row(w.kind, w.n + j) * w.K + w.k0) = o; }
; __device__ __forceinline__ void p0_weights(const Args& a, LAS unsigned char* lds) {
;     ...
;         else if ((r -= I_FD) < 16 * I_MG) { const int up = r / (8 * I_MG); r -= up * 8 * I_MG; const int e = r / I_MG; r -= e * I_MG; W = a.in[up ? I_MWU : I_MWG] + (size_t)e * D * DFE; w.K = D; w.N = DFE;
;             w.dst = a.ws + WS_MGU_T + (size_t)e * 2 * DFE * D * (MOE_FP8 ? 1 : 2); w.kind = 2 + up; w.f8 = MOE_FP8; w.scale = F8_WGU; }
;         else { r -= 16 * I_MG; const int e = r / I_MD; r -= e * I_MD; W = a.in[I_MWD] + (size_t)e * DFE * D; w.K = DFE; w.N = D; w.dst = a.ws + WS_MD_T + (size_t)e * D * DFE * (MOE_FP8 ? 1 : 2); w.f8 = MOE_FP8; w.scale = F8_WD; }
;         const int nblk = (w.N + 31) >> 5, kb = r / nblk, nb = r - kb * nblk;
;         w.k0 = 128 * kb + 16 * (lane >> 3); w.n = 32 * nb + 4 * (lane & 7); w.valid = w.n < w.N; w.src = W + (size_t)w.k0 * w.N + w.n;
.Lcn_wd_n0:
	s_bitcmp1_b32 s25, 31
	s_cbranch_scc0 .Lcn_snone_n0l
	s_and_b32 s12, s25, 0xfffffff
	s_lshr_b32 s13, s12, 2
	s_lshl_b32 s13, s13, 11
	s_add_u32 s13, s13, s100
	s_lshr_b32 s65, s13, 9
	s_mul_i32 s65, s65, 0x2493
	s_lshr_b32 s65, s65, 16
	s_mul_i32 s32, s65, 0xe00
	s_sub_u32 s13, s13, s32
	s_and_b32 s12, s12, 3
	s_cmp_ge_u32 s65, 16
	s_cbranch_scc1 .Lcn_dn_n0ld
	s_lshr_b32 s32, s13, 5
	s_mul_i32 s32, s32, 0x2493
	s_lshr_b32 s32, s32, 16
	s_mul_i32 s33, s32, 0xe0
	s_sub_u32 s33, s13, s33
	s_lshl_b32 s32, s32, 2
	s_add_u32 s32, s32, s12
	s_lshr_b32 s13, s65, 1
	s_and_b32 s65, s65, 1
	s_mul_i32 s12, s13, 0x1c00000
	s_add_u32 s12, s12, 0x4a000000
	s_lshr_b32 s13, s33, 2
	s_lshl_b32 s13, s13, 8
	s_lshl_b32 s65, s65, 7
	s_add_u32 s13, s13, s65
	s_and_b32 s65, s33, 3
	s_lshl_b32 s65, s65, 5
	s_add_u32 s13, s13, s65
	s_lshl_b32 s13, s13, 11
	s_add_u32 s12, s12, s13
	s_lshl_b32 s13, s32, 5
	s_add_u32 s12, s12, s13
	v_readlane_b32 s32, v255, 52
	v_readlane_b32 s33, v255, 53
	s_add_u32 s32, s32, s12
	s_addc_u32 s33, s33, 0
	s_movk_i32 s65, 0x800
	s_mov_b32 s13, 0x42000000
	s_branch .Lcn_dd_n0ld
.Lcn_dn_n0ld:
	s_lshr_b32 s32, s13, 6
	s_and_b32 s33, s13, 63
	s_lshl_b32 s32, s32, 2
	s_add_u32 s32, s32, s12
	s_sub_u32 s13, s65, 16
	s_mul_i32 s12, s13, 0xe00000
	s_add_u32 s12, s12, 0x66000000
	s_mul_i32 s13, s33, 0x38000
	s_add_u32 s12, s12, s13
	s_lshl_b32 s13, s32, 5
	s_add_u32 s12, s12, s13
	v_readlane_b32 s32, v255, 52
	v_readlane_b32 s33, v255, 53
	s_add_u32 s32, s32, s12
	s_addc_u32 s33, s33, 0
	s_movk_i32 s65, 0x1c00
	s_mov_b32 s13, 0x43000000
.Lcn_dd_n0ld:
	v_mul_f32_e32 v212, s13, v212
	v_mul_f32_e32 v213, s13, v213
	v_mul_f32_e32 v214, s13, v214
	v_mul_f32_e32 v215, s13, v215
	v_mul_f32_e32 v216, s13, v216
	v_mul_f32_e32 v217, s13, v217
	v_mul_f32_e32 v218, s13, v218
	v_mul_f32_e32 v219, s13, v219
	v_mul_f32_e32 v220, s13, v220
	v_mul_f32_e32 v221, s13, v221
	v_mul_f32_e32 v222, s13, v222
	v_mul_f32_e32 v223, s13, v223
	v_mul_f32_e32 v224, s13, v224
	v_mul_f32_e32 v225, s13, v225
	v_mul_f32_e32 v253, s13, v253
	v_mul_f32_e32 v254, s13, v254
	v_cvt_pk_fp8_f32 v212, v212, v216
	v_cvt_pk_fp8_f32 v213, v213, v217
	v_cvt_pk_fp8_f32 v214, v214, v218
	v_cvt_pk_fp8_f32 v215, v215, v219
	v_cvt_pk_fp8_f32 v212, v220, v224 op_sel:[0,0,1]
	v_cvt_pk_fp8_f32 v213, v221, v225 op_sel:[0,0,1]
	v_cvt_pk_fp8_f32 v214, v222, v253 op_sel:[0,0,1]
	v_cvt_pk_fp8_f32 v215, v223, v254 op_sel:[0,0,1]
	s_and_b32 s12, s25, 3
	v_and_b32_e32 v216, 63, v0
	v_and_b32_e32 v217, 7, v216
	v_lshrrev_b32_e32 v216, 3, v216
	v_and_b32_e32 v218, 3, v217
	v_xor_b32_e32 v218, s12, v218
	v_lshlrev_b32_e32 v218, 5, v218
	v_lshl_add_u32 v218, v216, 2, v218
	v_lshl_add_u32 v218, v217, 9, v218
	v_and_b32_e32 v219, 0x1c0, v0
	v_lshl_add_u32 v218, v219, 6, v218
	v_add_u32_e32 v218, 0x1c000, v218
	ds_write_b32 v218, v212 offset:0
	ds_write_b32 v218, v213 offset:128
	ds_write_b32 v218, v214 offset:256
	ds_write_b32 v218, v215 offset:384
	s_mov_b32 s67, s25
	s_mov_b32 s25, 0
.Lcn_snone_n0l:
	s_and_b32 s12, s67, 0x80000003
	s_cmp_eq_u32 s12, 0x80000003
	s_cbranch_scc0 .Lcn_fnone_n0l
	s_bitcmp1_b32 s67, 31
	s_cbranch_scc0 .Lcn_fnone_n0l
	s_and_b32 s12, s67, 0xfffffff
	s_lshr_b32 s13, s12, 2
	s_lshl_b32 s13, s13, 11
	s_add_u32 s13, s13, s100
	s_lshr_b32 s65, s13, 9
	s_mul_i32 s65, s65, 0x2493
	s_lshr_b32 s65, s65, 16
	s_mul_i32 s32, s65, 0xe00
	s_sub_u32 s13, s13, s32
	s_mov_b32 s12, 0
	s_cmp_ge_u32 s65, 16
	s_cbranch_scc1 .Lcn_dn_n0lf
	s_lshr_b32 s32, s13, 5
	s_mul_i32 s32, s32, 0x2493
	s_lshr_b32 s32, s32, 16
	s_mul_i32 s33, s32, 0xe0
	s_sub_u32 s33, s13, s33
	s_lshl_b32 s32, s32, 2
	s_add_u32 s32, s32, s12
	s_lshr_b32 s13, s65, 1
	s_and_b32 s65, s65, 1
	s_mul_i32 s12, s13, 0x1c00000
	s_add_u32 s12, s12, 0x4a000000
	s_lshr_b32 s13, s33, 2
	s_lshl_b32 s13, s13, 8
	s_lshl_b32 s65, s65, 7
	s_add_u32 s13, s13, s65
	s_and_b32 s65, s33, 3
	s_lshl_b32 s65, s65, 5
	s_add_u32 s13, s13, s65
	s_lshl_b32 s13, s13, 11
	s_add_u32 s12, s12, s13
	s_lshl_b32 s13, s32, 5
	s_add_u32 s12, s12, s13
	v_readlane_b32 s32, v255, 52
	v_readlane_b32 s33, v255, 53
	s_add_u32 s32, s32, s12
	s_addc_u32 s33, s33, 0
	s_movk_i32 s65, 0x800
	s_mov_b32 s13, 0x42000000
	s_branch .Lcn_dd_n0lf

; __device__ __forceinline__ unsigned pk4_fp8(float a, float b, float c, float d) { int p = __builtin_amdgcn_cvt_pk_fp8_f32(a, b, 0, false); p = __builtin_amdgcn_cvt_pk_fp8_f32(c, d, p, true); return (unsigned)p; }
; __device__ __forceinline__ void witem_store(const WItem& w, const f32x4 (&v)[16]) {
;     if (!w.valid) return;
;     if (w.f8) {
; #pragma unroll
;         for (int j = 0; j < 4; ++j) { u32x4 o; const float sc = w.scale;
;             o.x = pk4_fp8(v[0][j] * sc, v[1][j] * sc, v[2][j] * sc, v[3][j] * sc); o.y = pk4_fp8(v[4][j] * sc, v[5][j] * sc, v[6][j] * sc, v[7][j] * sc);
;             o.z = pk4_fp8(v[8][j] * sc, v[9][j] * sc, v[10][j] * sc, v[11][j] * sc); o.w = pk4_fp8(v[12][j] * sc, v[13][j] * sc, v[14][j] * sc, v[15][j] * sc);
;             *(u32x4*)(w.dst + (size_t)witem_row(w.kind, w.n + j) * w.K + w.k0) = o; }
; __device__ __forceinline__ void p0_weights(const Args& a, LAS unsigned char* lds) {
;     ...
;     { f32x4 v[16], vn[16];
;       WItem cur = decode(gw); witem_load(cur, v);
; #pragma unroll 1
;       for (int it = gw; it < NIT; it += NGW) {
;           const WItem nxt = decode(it + NGW); witem_load(nxt, vn);
;           __builtin_amdgcn_sched_barrier(0);
;           witem_store(cur, v);
;           __builtin_amdgcn_sched_barrier(0);
; #pragma unroll
;           for (int i = 0; i < 16; ++i) v[i] = vn[i];
;           cur = nxt; } }
.Lcn_dd_n0lf:
	s_lshr_b32 s12, s101, 28
	s_and_b32 s12, s12, 3
	s_and_b32 s13, s67, 3
	s_add_u32 s13, s13, 1
	s_sub_u32 s13, s13, s12
	v_and_b32_e32 v224, 63, v0
	v_lshrrev_b32_e32 v225, 3, v224
	v_and_b32_e32 v224, 7, v224
	v_lshrrev_b32_e32 v253, 1, v224
	v_subrev_u32_e32 v254, s12, v253
	v_cmp_gt_u32_e64 s[12:13], s13, v254
	v_lshrrev_b32_e32 v254, 2, v225
	v_xor_b32_e32 v254, v254, v253
	v_lshlrev_b32_e32 v254, 1, v254
	v_and_b32_e32 v253, 1, v224
	v_or_b32_e32 v254, v254, v253
	v_lshlrev_b32_e32 v254, 4, v254
	v_lshl_add_u32 v254, v225, 7, v254
	v_and_b32_e32 v253, 0x1c0, v0
	v_lshl_add_u32 v254, v253, 6, v254
	v_add_u32_e32 v254, 0x1c000, v254
	v_xor_b32_e32 v253, 64, v254
	v_mul_u32_u24_e32 v225, s65, v225
	v_lshl_add_u32 v225, v224, 4, v225
	s_mov_b64 exec, s[12:13]
	ds_read_b128 v[212:215], v254
	ds_read_b128 v[216:219], v253 offset:1024
	ds_read_b128 v[220:223], v254 offset:2048
	s_lshl_b32 s65, s65, 3
	s_waitcnt lgkmcnt(0)
	global_store_dwordx4 v225, v[212:215], s[32:33] nt
	s_add_u32 s32, s32, s65
	s_addc_u32 s33, s33, 0
	s_nop 1
	ds_read_b128 v[212:215], v253 offset:3072
	global_store_dwordx4 v225, v[216:219], s[32:33] nt
	s_add_u32 s32, s32, s65
	s_addc_u32 s33, s33, 0
	global_store_dwordx4 v225, v[220:223], s[32:33] nt
	s_add_u32 s32, s32, s65
	s_addc_u32 s33, s33, 0
	s_waitcnt lgkmcnt(0)
	global_store_dwordx4 v225, v[212:215], s[32:33] nt
	s_mov_b64 exec, -1
	s_and_b32 s65, s67, 3
	s_add_u32 s65, s65, 1
	s_and_b32 s65, s65, 3
	s_lshl_b32 s65, s65, 28
	s_andn2_b32 s101, s101, 0x30000000
	s_or_b32 s101, s101, s65
	s_mov_b32 s67, 0
.Lcn_fnone_n0l:
	s_mov_b32 s25, 0
	s_cmp_gt_i32 s74, s15
	s_cbranch_scc1 .Lcn_lskip_n0l
	s_and_b32 s12, s101, 0xfffffff
	s_cmp_ge_u32 s12, 168
	s_cbranch_scc1 .Lcn_ldum_n0l
	s_and_b32 s12, s101, 0xfffffff
	s_lshr_b32 s13, s12, 2
	s_lshl_b32 s13, s13, 11
	s_add_u32 s13, s13, s100
	s_lshr_b32 s65, s13, 9
	s_mul_i32 s65, s65, 0x2493
	s_lshr_b32 s65, s65, 16
	s_mul_i32 s32, s65, 0xe00
	s_sub_u32 s13, s13, s32
	s_and_b32 s12, s12, 3
	s_cmp_ge_u32 s65, 16
	s_cbranch_scc1 .Lcn_dn_n0ls
	s_lshr_b32 s32, s13, 5
	s_mul_i32 s32, s32, 0x2493
	s_lshr_b32 s32, s32, 16
	s_mul_i32 s33, s32, 0xe0
	s_sub_u32 s33, s13, s33
	s_lshl_b32 s32, s32, 2
	s_add_u32 s32, s32, s12
	s_lshr_b32 s13, s65, 1
	s_and_b32 s65, s65, 1
	s_mul_i32 s12, s13, 0x3800000
	s_mul_i32 s13, s32, 0xe0000
	s_add_u32 s12, s12, s13
	s_lshl_b32 s13, s33, 7
	s_add_u32 s12, s12, s13
	v_readlane_b32 s32, v255, 46
	v_readlane_b32 s33, v255, 47
	s_cmp_eq_u32 s65, 0
	s_cselect_b32 s32, s98, s32
	s_cselect_b32 s33, s99, s33
	s_add_u32 s32, s32, s12
	s_addc_u32 s33, s33, 0
	s_movk_i32 s65, 0x7000
	s_branch .Lcn_dd_n0ls

; __device__ __forceinline__ void witem_load(const WItem& w, f32x4 (&v)[16]) {
;     if (!w.valid) return;
; #pragma unroll
;     for (int i = 0; i < 16; ++i) v[i] = *(const f32x4*)(w.src + (size_t)i * w.N);
; }
.Lcn_lgo_n0l:
	v_and_b32_e32 v224, 63, v0
	v_and_b32_e32 v253, 7, v224
	v_lshrrev_b32_e32 v224, 3, v224
	v_lshlrev_b32_e32 v224, 2, v224
	v_lshlrev_b32_e32 v225, 4, v253
	v_lshlrev_b32_e32 v253, 2, v253
	v_mad_u32_u24 v254, v224, s65, v225
	global_load_dwordx4 v[212:215], v254, s[32:33] nt
	s_add_u32 s32, s32, s65
	s_addc_u32 s33, s33, 0
	global_load_dwordx4 v[216:219], v254, s[32:33] nt
	s_add_u32 s32, s32, s65
	s_addc_u32 s33, s33, 0
	global_load_dwordx4 v[220:223], v254, s[32:33] nt
	s_add_u32 s32, s32, s65
	s_addc_u32 s33, s33, 0
	global_load_dwordx2 v[224:225], v254, s[32:33] offset:0 nt
	global_load_dword v253, v254, s[32:33] offset:8 nt
	global_load_dword v254, v254, s[32:33] offset:12 nt

; __device__ __forceinline__ unsigned pk4_fp8(float a, float b, float c, float d) { int p = __builtin_amdgcn_cvt_pk_fp8_f32(a, b, 0, false); p = __builtin_amdgcn_cvt_pk_fp8_f32(c, d, p, true); return (unsigned)p; }
; __device__ __forceinline__ void witem_store(const WItem& w, const f32x4 (&v)[16]) {
;     if (!w.valid) return;
;     if (w.f8) {
; #pragma unroll
;         for (int j = 0; j < 4; ++j) { u32x4 o; const float sc = w.scale;
;             o.x = pk4_fp8(v[0][j] * sc, v[1][j] * sc, v[2][j] * sc, v[3][j] * sc); o.y = pk4_fp8(v[4][j] * sc, v[5][j] * sc, v[6][j] * sc, v[7][j] * sc);
;             o.z = pk4_fp8(v[8][j] * sc, v[9][j] * sc, v[10][j] * sc, v[11][j] * sc); o.w = pk4_fp8(v[12][j] * sc, v[13][j] * sc, v[14][j] * sc, v[15][j] * sc);
;             *(u32x4*)(w.dst + (size_t)witem_row(w.kind, w.n + j) * w.K + w.k0) = o; }
; __device__ __forceinline__ void p0_weights(const Args& a, LAS unsigned char* lds) {
;     ...
;         else if ((r -= I_FD) < 16 * I_MG) { const int up = r / (8 * I_MG); r -= up * 8 * I_MG; const int e = r / I_MG; r -= e * I_MG; W = a.in[up ? I_MWU : I_MWG] + (size_t)e * D * DFE; w.K = D; w.N = DFE;
;             w.dst = a.ws + WS_MGU_T + (size_t)e * 2 * DFE * D * (MOE_FP8 ? 1 : 2); w.kind = 2 + up; w.f8 = MOE_FP8; w.scale = F8_WGU; }
;         else { r -= 16 * I_MG; const int e = r / I_MD; r -= e * I_MD; W = a.in[I_MWD] + (size_t)e * DFE * D; w.K = DFE; w.N = D; w.dst = a.ws + WS_MD_T + (size_t)e * D * DFE * (MOE_FP8 ? 1 : 2); w.f8 = MOE_FP8; w.scale = F8_WD; }
;         const int nblk = (w.N + 31) >> 5, kb = r / nblk, nb = r - kb * nblk;
;         w.k0 = 128 * kb + 16 * (lane >> 3); w.n = 32 * nb + 4 * (lane & 7); w.valid = w.n < w.N; w.src = W + (size_t)w.k0 * w.N + w.n;
.Lcn_exit_n0:
	s_bitcmp1_b32 s25, 31
	s_cbranch_scc0 .Lcn_xnone_n0
	s_waitcnt vmcnt(0)
	s_bitcmp1_b32 s25, 31
	s_cbranch_scc0 .Lcn_snone_n0x
	s_and_b32 s12, s25, 0xfffffff
	s_lshr_b32 s13, s12, 2
	s_lshl_b32 s13, s13, 11
	s_add_u32 s13, s13, s100
	s_lshr_b32 s65, s13, 9
	s_mul_i32 s65, s65, 0x2493
	s_lshr_b32 s65, s65, 16
	s_mul_i32 s32, s65, 0xe00
	s_sub_u32 s13, s13, s32
	s_and_b32 s12, s12, 3
	s_cmp_ge_u32 s65, 16
	s_cbranch_scc1 .Lcn_dn_n0xd
	s_lshr_b32 s32, s13, 5
	s_mul_i32 s32, s32, 0x2493
	s_lshr_b32 s32, s32, 16
	s_mul_i32 s33, s32, 0xe0
	s_sub_u32 s33, s13, s33
	s_lshl_b32 s32, s32, 2
	s_add_u32 s32, s32, s12
	s_lshr_b32 s13, s65, 1
	s_and_b32 s65, s65, 1
	s_mul_i32 s12, s13, 0x1c00000
	s_add_u32 s12, s12, 0x4a000000
	s_lshr_b32 s13, s33, 2
	s_lshl_b32 s13, s13, 8
	s_lshl_b32 s65, s65, 7
	s_add_u32 s13, s13, s65
	s_and_b32 s65, s33, 3
	s_lshl_b32 s65, s65, 5
	s_add_u32 s13, s13, s65
	s_lshl_b32 s13, s13, 11
	s_add_u32 s12, s12, s13
	s_lshl_b32 s13, s32, 5
	s_add_u32 s12, s12, s13
	v_readlane_b32 s32, v255, 52
	v_readlane_b32 s33, v255, 53
	s_add_u32 s32, s32, s12
	s_addc_u32 s33, s33, 0
	s_movk_i32 s65, 0x800
	s_mov_b32 s13, 0x42000000
	s_branch .Lcn_dd_n0xd

; __device__ __forceinline__ unsigned pk4_fp8(float a, float b, float c, float d) { int p = __builtin_amdgcn_cvt_pk_fp8_f32(a, b, 0, false); p = __builtin_amdgcn_cvt_pk_fp8_f32(c, d, p, true); return (unsigned)p; }
; __device__ __forceinline__ void witem_store(const WItem& w, const f32x4 (&v)[16]) {
;     if (!w.valid) return;
;     if (w.f8) {
; #pragma unroll
;         for (int j = 0; j < 4; ++j) { u32x4 o; const float sc = w.scale;
;             o.x = pk4_fp8(v[0][j] * sc, v[1][j] * sc, v[2][j] * sc, v[3][j] * sc); o.y = pk4_fp8(v[4][j] * sc, v[5][j] * sc, v[6][j] * sc, v[7][j] * sc);
;             o.z = pk4_fp8(v[8][j] * sc, v[9][j] * sc, v[10][j] * sc, v[11][j] * sc); o.w = pk4_fp8(v[12][j] * sc, v[13][j] * sc, v[14][j] * sc, v[15][j] * sc);
;             *(u32x4*)(w.dst + (size_t)witem_row(w.kind, w.n + j) * w.K + w.k0) = o; }
; __device__ __forceinline__ void p0_weights(const Args& a, LAS unsigned char* lds) {
;     ...
;         else if ((r -= I_FD) < 16 * I_MG) { const int up = r / (8 * I_MG); r -= up * 8 * I_MG; const int e = r / I_MG; r -= e * I_MG; W = a.in[up ? I_MWU : I_MWG] + (size_t)e * D * DFE; w.K = D; w.N = DFE;
;             w.dst = a.ws + WS_MGU_T + (size_t)e * 2 * DFE * D * (MOE_FP8 ? 1 : 2); w.kind = 2 + up; w.f8 = MOE_FP8; w.scale = F8_WGU; }
;         else { r -= 16 * I_MG; const int e = r / I_MD; r -= e * I_MD; W = a.in[I_MWD] + (size_t)e * DFE * D; w.K = DFE; w.N = D; w.dst = a.ws + WS_MD_T + (size_t)e * D * DFE * (MOE_FP8 ? 1 : 2); w.f8 = MOE_FP8; w.scale = F8_WD; }
;         const int nblk = (w.N + 31) >> 5, kb = r / nblk, nb = r - kb * nblk;
;         w.k0 = 128 * kb + 16 * (lane >> 3); w.n = 32 * nb + 4 * (lane & 7); w.valid = w.n < w.N; w.src = W + (size_t)w.k0 * w.N + w.n;
.Lcn_snone_n0x:
.Lcn_xnone_n0:
	s_bitcmp1_b32 s67, 31
	s_cbranch_scc0 .Lcn_fnone_n0x
	s_and_b32 s12, s67, 0xfffffff
	s_lshr_b32 s13, s12, 2
	s_lshl_b32 s13, s13, 11
	s_add_u32 s13, s13, s100
	s_lshr_b32 s65, s13, 9
	s_mul_i32 s65, s65, 0x2493
	s_lshr_b32 s65, s65, 16
	s_mul_i32 s32, s65, 0xe00
	s_sub_u32 s13, s13, s32
	s_mov_b32 s12, 0
	s_cmp_ge_u32 s65, 16
	s_cbranch_scc1 .Lcn_dn_n0xf
	s_lshr_b32 s32, s13, 5
	s_mul_i32 s32, s32, 0x2493
	s_lshr_b32 s32, s32, 16
	s_mul_i32 s33, s32, 0xe0
	s_sub_u32 s33, s13, s33
	s_lshl_b32 s32, s32, 2
	s_add_u32 s32, s32, s12
	s_lshr_b32 s13, s65, 1
	s_and_b32 s65, s65, 1
	s_mul_i32 s12, s13, 0x1c00000
	s_add_u32 s12, s12, 0x4a000000
	s_lshr_b32 s13, s33, 2
	s_lshl_b32 s13, s13, 8
	s_lshl_b32 s65, s65, 7
	s_add_u32 s13, s13, s65
	s_and_b32 s65, s33, 3
	s_lshl_b32 s65, s65, 5
	s_add_u32 s13, s13, s65
	s_lshl_b32 s13, s13, 11
	s_add_u32 s12, s12, s13
	s_lshl_b32 s13, s32, 5
	s_add_u32 s12, s12, s13
	v_readlane_b32 s32, v255, 52
	v_readlane_b32 s33, v255, 53
	s_add_u32 s32, s32, s12
	s_addc_u32 s33, s33, 0
	s_movk_i32 s65, 0x800
	s_mov_b32 s13, 0x42000000
	s_branch .Lcn_dd_n0xf

; __device__ __forceinline__ void p0_weights(const Args& a, LAS unsigned char* lds) {
;     ...
;         else if ((r -= I_FD) < 16 * I_MG) { const int up = r / (8 * I_MG); r -= up * 8 * I_MG; const int e = r / I_MG; r -= e * I_MG; W = a.in[up ? I_MWU : I_MWG] + (size_t)e * D * DFE; w.K = D; w.N = DFE;
;             w.dst = a.ws + WS_MGU_T + (size_t)e * 2 * DFE * D * (MOE_FP8 ? 1 : 2); w.kind = 2 + up; w.f8 = MOE_FP8; w.scale = F8_WGU; }
;         else { r -= 16 * I_MG; const int e = r / I_MD; r -= e * I_MD; W = a.in[I_MWD] + (size_t)e * DFE * D; w.K = DFE; w.N = D; w.dst = a.ws + WS_MD_T + (size_t)e * D * DFE * (MOE_FP8 ? 1 : 2); w.f8 = MOE_FP8; w.scale = F8_WD; }
;         const int nblk = (w.N + 31) >> 5, kb = r / nblk, nb = r - kb * nblk;
;         w.k0 = 128 * kb + 16 * (lane >> 3); w.n = 32 * nb + 4 * (lane & 7); w.valid = w.n < w.N; w.src = W + (size_t)w.k0 * w.N + w.n;
; __device__ __forceinline__ void nsa_unit(const Args& a, LAS unsigned char* lds, int b, int kvh, int qb) {
;     ...
; #pragma unroll
;     for (int dt = 0; dt < 4; ++dt)
; #pragma unroll
;         for (int i = 0; i < 16; ++i) o[dt][i] = 0.f;
;     float mrun = -1e30f, lrun = 0.f;
;     f32x16 p0, p1;
; #pragma unroll
;     for (int i = 0; i < 16; ++i) { p0[i] = 0.f; p1[i] = 0.f; }
;     bf16x8 pf[2][2];
;     if (w >= 4) asm volatile("s_barrier" ::: "memory");
.LBB0_1840:
	s_cmp_lt_i32 s17, -1
	s_cbranch_scc1 .LBB0_1865
	v_mov_b32_e32 v49, v47
	s_lshl_b32 s0, s62, 1
	s_max_i32 s1, s62, 8
	v_mov_b32_e32 v60, v47
	v_mov_b32_e32 v61, v47
	v_lshl_add_u64 v[206:207], s[30:31], 0, v[48:49]
	s_sub_i32 s69, s0, s1
	v_mov_b32_e32 v46, v47
	v_mov_b32_e32 v48, v47
	v_mov_b32_e32 v50, v47
	v_mov_b32_e32 v51, v47
	v_mov_b32_e32 v52, v47
	v_mov_b32_e32 v53, v47
	v_mov_b32_e32 v54, v47
	v_mov_b32_e32 v55, v47
	v_mov_b32_e32 v56, v47
	v_mov_b32_e32 v57, v47
	v_mov_b32_e32 v58, v47
	v_mov_b32_e32 v59, v47
	v_mov_b64_e32 v[108:109], v[60:61]
	v_mov_b64_e32 v[124:125], v[60:61]
	v_mov_b64_e32 v[140:141], v[60:61]
	v_mov_b64_e32 v[156:157], v[60:61]
	v_mov_b64_e32 v[76:77], v[60:61]
	v_mov_b64_e32 v[92:93], v[60:61]
	v_add_u32_e32 v43, 1, v249
	s_add_i32 s56, s69, 11
	s_add_i32 s57, s69, 10
	s_mov_b32 s68, 2
	s_add_i32 s69, s69, 2
	s_mov_b32 s70, 0
	v_mov_b32_e32 v208, 0xf149f2ca
	v_mov_b32_e32 v209, 0
	s_movk_i32 s71, 0xc000
	v_mov_b64_e32 v[106:107], v[58:59]
	v_mov_b64_e32 v[104:105], v[56:57]
	v_mov_b64_e32 v[102:103], v[54:55]
	v_mov_b64_e32 v[100:101], v[52:53]
	v_mov_b64_e32 v[98:99], v[50:51]
	v_mov_b64_e32 v[96:97], v[48:49]
	v_mov_b64_e32 v[94:95], v[46:47]
	v_mov_b64_e32 v[122:123], v[58:59]
	v_mov_b64_e32 v[120:121], v[56:57]
	v_mov_b64_e32 v[118:119], v[54:55]
	v_mov_b64_e32 v[116:117], v[52:53]
	v_mov_b64_e32 v[114:115], v[50:51]
	v_mov_b64_e32 v[112:113], v[48:49]
	v_mov_b64_e32 v[110:111], v[46:47]
	v_mov_b64_e32 v[138:139], v[58:59]
	v_mov_b64_e32 v[136:137], v[56:57]
	v_mov_b64_e32 v[134:135], v[54:55]
	v_mov_b64_e32 v[132:133], v[52:53]
	v_mov_b64_e32 v[130:131], v[50:51]
	v_mov_b64_e32 v[128:129], v[48:49]
	v_mov_b64_e32 v[126:127], v[46:47]
	v_mov_b64_e32 v[154:155], v[58:59]
	v_mov_b64_e32 v[152:153], v[56:57]
	v_mov_b64_e32 v[150:151], v[54:55]
	v_mov_b64_e32 v[148:149], v[52:53]
	v_mov_b64_e32 v[146:147], v[50:51]
	v_mov_b64_e32 v[144:145], v[48:49]
	v_mov_b64_e32 v[142:143], v[46:47]
	v_mov_b64_e32 v[74:75], v[58:59]
	v_mov_b64_e32 v[72:73], v[56:57]
	v_mov_b64_e32 v[70:71], v[54:55]
	v_mov_b64_e32 v[68:69], v[52:53]
	v_mov_b64_e32 v[66:67], v[50:51]
	v_mov_b64_e32 v[64:65], v[48:49]
	v_mov_b64_e32 v[62:63], v[46:47]
	v_mov_b64_e32 v[90:91], v[58:59]
	v_mov_b64_e32 v[88:89], v[56:57]
	v_mov_b64_e32 v[86:87], v[54:55]
	v_mov_b64_e32 v[84:85], v[52:53]
	v_mov_b64_e32 v[82:83], v[50:51]
	v_mov_b64_e32 v[80:81], v[48:49]
	v_mov_b64_e32 v[78:79], v[46:47]
	s_mov_b32 s67, 0
	s_and_b32 s14, s101, 3
	s_lshl_b32 s14, s14, 28
	s_andn2_b32 s101, s101, 0x30000000
	s_or_b32 s101, s101, s14
	s_and_b32 s14, s101, 0xfffffff
	s_cmp_ge_u32 s14, 168
	s_cbranch_scc1 .Lcn_ldum_n1s
	s_and_b32 s14, s101, 0xfffffff
	s_lshr_b32 s15, s14, 2
	s_lshl_b32 s15, s15, 11
	s_add_u32 s15, s15, s100
	s_lshr_b32 vcc_lo, s15, 9
	s_mul_i32 vcc_lo, vcc_lo, 0x2493
	s_lshr_b32 vcc_lo, vcc_lo, 16
	s_mul_i32 s32, vcc_lo, 0xe00
	s_sub_u32 s15, s15, s32
	s_and_b32 s14, s14, 3
	s_cmp_ge_u32 vcc_lo, 16
	s_cbranch_scc1 .Lcn_dn_n1ss
	s_lshr_b32 s32, s15, 5
	s_mul_i32 s32, s32, 0x2493
	s_lshr_b32 s32, s32, 16
	s_mul_i32 s33, s32, 0xe0
	s_sub_u32 s33, s15, s33
	s_lshl_b32 s32, s32, 2
	s_add_u32 s32, s32, s14
	s_lshr_b32 s15, vcc_lo, 1
	s_and_b32 vcc_lo, vcc_lo, 1
	s_mul_i32 s14, s15, 0x3800000
	s_mul_i32 s15, s32, 0xe0000
	s_add_u32 s14, s14, s15
	s_lshl_b32 s15, s33, 7
	s_add_u32 s14, s14, s15
	v_readlane_b32 s32, v255, 46
	v_readlane_b32 s33, v255, 47
	s_cmp_eq_u32 vcc_lo, 0
	s_cselect_b32 s32, s98, s32
	s_cselect_b32 s33, s99, s33
	s_add_u32 s32, s32, s14
	s_addc_u32 s33, s33, 0
	s_movk_i32 vcc_lo, 0x7000
	s_branch .Lcn_dd_n1ss
.Lcn_dn_n1ss:
	s_lshr_b32 s32, s15, 6
	s_and_b32 s33, s15, 63
	s_lshl_b32 s32, s32, 2
	s_add_u32 s32, s32, s14
	s_sub_u32 s15, vcc_lo, 16
	s_mul_i32 s14, s15, 0x3800000
	s_lshl_b32 s15, s32, 18
	s_add_u32 s14, s14, s15
	s_lshl_b32 s15, s33, 7
	s_add_u32 s14, s14, s15
	v_readlane_b32 s32, v255, 48
	v_readlane_b32 s33, v255, 49
	s_add_u32 s32, s32, s14
	s_addc_u32 s33, s33, 0
	s_movk_i32 vcc_lo, 0x2000

; __device__ __forceinline__ void witem_load(const WItem& w, f32x4 (&v)[16]) {
;     if (!w.valid) return;
; #pragma unroll
;     for (int i = 0; i < 16; ++i) v[i] = *(const f32x4*)(w.src + (size_t)i * w.N);
; }
.Lcn_ldum_n1s:
	v_readlane_b32 s32, v255, 52
	v_readlane_b32 s33, v255, 53
	s_add_u32 s32, s32, 0x500000
	s_addc_u32 s33, s33, 0
	s_movk_i32 vcc_lo, 0x2000
	s_mov_b32 s25, 0
.Lcn_lgo_n1s:
	v_and_b32_e32 v220, 63, v0
	v_and_b32_e32 v253, 7, v220
	v_lshrrev_b32_e32 v220, 3, v220
	v_lshlrev_b32_e32 v220, 2, v220
	v_lshlrev_b32_e32 v221, 4, v253
	v_lshlrev_b32_e32 v253, 2, v253
	v_mad_u32_u24 v254, v220, vcc_lo, v221
	global_load_dwordx4 v[212:215], v254, s[32:33] nt
	s_add_u32 s32, s32, vcc_lo
	s_addc_u32 s33, s33, 0
	global_load_dwordx4 v[216:219], v254, s[32:33] nt
	s_add_u32 s32, s32, vcc_lo
	s_addc_u32 s33, s33, 0
	global_load_dwordx4 v[224:227], v254, s[32:33] nt
	s_add_u32 s32, s32, vcc_lo
	s_addc_u32 s33, s33, 0
	global_load_dwordx2 v[220:221], v254, s[32:33] offset:0 nt
	global_load_dword v253, v254, s[32:33] offset:8 nt
	global_load_dword v254, v254, s[32:33] offset:12 nt
	s_branch .LBB0_1843

; __device__ __forceinline__ void nsa_unit(const Args& a, LAS unsigned char* lds, int b, int kvh, int qb) {
;     ...
;         if (it + 1 < nTot) asm volatile("s_waitcnt vmcnt(4) lgkmcnt(0)\n\ts_barrier" ::: "memory"); else asm volatile("s_waitcnt vmcnt(0) lgkmcnt(0)\n\ts_barrier" ::: "memory");
;         if (it > 0) { const int ti = it - 1;
.LBB0_1848:
	s_add_i32 s14, s70, 1
	s_cmp_gt_i32 s14, s17
	s_cbranch_scc1 .Lcn_w0_n1
	s_waitcnt vmcnt(4)
	s_branch .Lcn_wd_n1

; __device__ __forceinline__ unsigned pk4_fp8(float a, float b, float c, float d) { int p = __builtin_amdgcn_cvt_pk_fp8_f32(a, b, 0, false); p = __builtin_amdgcn_cvt_pk_fp8_f32(c, d, p, true); return (unsigned)p; }
; __device__ __forceinline__ void witem_store(const WItem& w, const f32x4 (&v)[16]) {
;     if (!w.valid) return;
;     if (w.f8) {
; #pragma unroll
;         for (int j = 0; j < 4; ++j) { u32x4 o; const float sc = w.scale;
;             o.x = pk4_fp8(v[0][j] * sc, v[1][j] * sc, v[2][j] * sc, v[3][j] * sc); o.y = pk4_fp8(v[4][j] * sc, v[5][j] * sc, v[6][j] * sc, v[7][j] * sc);
;             o.z = pk4_fp8(v[8][j] * sc, v[9][j] * sc, v[10][j] * sc, v[11][j] * sc); o.w = pk4_fp8(v[12][j] * sc, v[13][j] * sc, v[14][j] * sc, v[15][j] * sc);
;             *(u32x4*)(w.dst + (size_t)witem_row(w.kind, w.n + j) * w.K + w.k0) = o; }
; __device__ __forceinline__ void p0_weights(const Args& a, LAS unsigned char* lds) {
;     ...
;         else if ((r -= I_FD) < 16 * I_MG) { const int up = r / (8 * I_MG); r -= up * 8 * I_MG; const int e = r / I_MG; r -= e * I_MG; W = a.in[up ? I_MWU : I_MWG] + (size_t)e * D * DFE; w.K = D; w.N = DFE;
;             w.dst = a.ws + WS_MGU_T + (size_t)e * 2 * DFE * D * (MOE_FP8 ? 1 : 2); w.kind = 2 + up; w.f8 = MOE_FP8; w.scale = F8_WGU; }
;         else { r -= 16 * I_MG; const int e = r / I_MD; r -= e * I_MD; W = a.in[I_MWD] + (size_t)e * DFE * D; w.K = DFE; w.N = D; w.dst = a.ws + WS_MD_T + (size_t)e * D * DFE * (MOE_FP8 ? 1 : 2); w.f8 = MOE_FP8; w.scale = F8_WD; }
;         const int nblk = (w.N + 31) >> 5, kb = r / nblk, nb = r - kb * nblk;
;         w.k0 = 128 * kb + 16 * (lane >> 3); w.n = 32 * nb + 4 * (lane & 7); w.valid = w.n < w.N; w.src = W + (size_t)w.k0 * w.N + w.n;
.Lcn_wd_n1:
	s_bitcmp1_b32 s25, 31
	s_cbranch_scc0 .Lcn_snone_n1l
	s_and_b32 s14, s25, 0xfffffff
	s_lshr_b32 s15, s14, 2
	s_lshl_b32 s15, s15, 11
	s_add_u32 s15, s15, s100
	s_lshr_b32 vcc_lo, s15, 9
	s_mul_i32 vcc_lo, vcc_lo, 0x2493
	s_lshr_b32 vcc_lo, vcc_lo, 16
	s_mul_i32 s32, vcc_lo, 0xe00
	s_sub_u32 s15, s15, s32
	s_and_b32 s14, s14, 3
	s_cmp_ge_u32 vcc_lo, 16
	s_cbranch_scc1 .Lcn_dn_n1ld
	s_lshr_b32 s32, s15, 5
	s_mul_i32 s32, s32, 0x2493
	s_lshr_b32 s32, s32, 16
	s_mul_i32 s33, s32, 0xe0
	s_sub_u32 s33, s15, s33
	s_lshl_b32 s32, s32, 2
	s_add_u32 s32, s32, s14
	s_lshr_b32 s15, vcc_lo, 1
	s_and_b32 vcc_lo, vcc_lo, 1
	s_mul_i32 s14, s15, 0x1c00000
	s_add_u32 s14, s14, 0x4a000000
	s_lshr_b32 s15, s33, 2
	s_lshl_b32 s15, s15, 8
	s_lshl_b32 vcc_lo, vcc_lo, 7
	s_add_u32 s15, s15, vcc_lo
	s_and_b32 vcc_lo, s33, 3
	s_lshl_b32 vcc_lo, vcc_lo, 5
	s_add_u32 s15, s15, vcc_lo
	s_lshl_b32 s15, s15, 11
	s_add_u32 s14, s14, s15
	s_lshl_b32 s15, s32, 5
	s_add_u32 s14, s14, s15
	v_readlane_b32 s32, v255, 52
	v_readlane_b32 s33, v255, 53
	s_add_u32 s32, s32, s14
	s_addc_u32 s33, s33, 0
	s_movk_i32 vcc_lo, 0x800
	s_mov_b32 s15, 0x42000000
	s_branch .Lcn_dd_n1ld
.Lcn_dn_n1ld:
	s_lshr_b32 s32, s15, 6
	s_and_b32 s33, s15, 63
	s_lshl_b32 s32, s32, 2
	s_add_u32 s32, s32, s14
	s_sub_u32 s15, vcc_lo, 16
	s_mul_i32 s14, s15, 0xe00000
	s_add_u32 s14, s14, 0x66000000
	s_mul_i32 s15, s33, 0x38000
	s_add_u32 s14, s14, s15
	s_lshl_b32 s15, s32, 5
	s_add_u32 s14, s14, s15
	v_readlane_b32 s32, v255, 52
	v_readlane_b32 s33, v255, 53
	s_add_u32 s32, s32, s14
	s_addc_u32 s33, s33, 0
	s_movk_i32 vcc_lo, 0x1c00
	s_mov_b32 s15, 0x43000000
.Lcn_dd_n1ld:
	v_mul_f32_e32 v212, s15, v212
	v_mul_f32_e32 v213, s15, v213
	v_mul_f32_e32 v214, s15, v214
	v_mul_f32_e32 v215, s15, v215
	v_mul_f32_e32 v216, s15, v216
	v_mul_f32_e32 v217, s15, v217
	v_mul_f32_e32 v218, s15, v218
	v_mul_f32_e32 v219, s15, v219
	v_mul_f32_e32 v224, s15, v224
	v_mul_f32_e32 v225, s15, v225
	v_mul_f32_e32 v226, s15, v226
	v_mul_f32_e32 v227, s15, v227
	v_mul_f32_e32 v220, s15, v220
	v_mul_f32_e32 v221, s15, v221
	v_mul_f32_e32 v253, s15, v253
	v_mul_f32_e32 v254, s15, v254
	v_cvt_pk_fp8_f32 v212, v212, v216
	v_cvt_pk_fp8_f32 v213, v213, v217
	v_cvt_pk_fp8_f32 v214, v214, v218
	v_cvt_pk_fp8_f32 v215, v215, v219
	v_cvt_pk_fp8_f32 v212, v224, v220 op_sel:[0,0,1]
	v_cvt_pk_fp8_f32 v213, v225, v221 op_sel:[0,0,1]
	v_cvt_pk_fp8_f32 v214, v226, v253 op_sel:[0,0,1]
	v_cvt_pk_fp8_f32 v215, v227, v254 op_sel:[0,0,1]
	s_and_b32 s14, s25, 3
	v_and_b32_e32 v216, 63, v0
	v_and_b32_e32 v217, 7, v216
	v_lshrrev_b32_e32 v216, 3, v216
	v_and_b32_e32 v218, 3, v217
	v_xor_b32_e32 v218, s14, v218
	v_lshlrev_b32_e32 v218, 5, v218
	v_lshl_add_u32 v218, v216, 2, v218
	v_lshl_add_u32 v218, v217, 9, v218
	v_and_b32_e32 v219, 0x1c0, v0
	v_lshl_add_u32 v218, v219, 6, v218
	v_add_u32_e32 v218, 0x1c000, v218
	ds_write_b32 v218, v212 offset:0
	ds_write_b32 v218, v213 offset:128
	ds_write_b32 v218, v214 offset:256
	ds_write_b32 v218, v215 offset:384
	s_mov_b32 s67, s25
	s_mov_b32 s25, 0
.Lcn_snone_n1l:
	s_and_b32 s14, s67, 0x80000003
	s_cmp_eq_u32 s14, 0x80000003
	s_cbranch_scc0 .Lcn_fnone_n1l
	s_bitcmp1_b32 s67, 31
	s_cbranch_scc0 .Lcn_fnone_n1l
	s_and_b32 s14, s67, 0xfffffff
	s_lshr_b32 s15, s14, 2
	s_lshl_b32 s15, s15, 11
	s_add_u32 s15, s15, s100
	s_lshr_b32 vcc_lo, s15, 9
	s_mul_i32 vcc_lo, vcc_lo, 0x2493
	s_lshr_b32 vcc_lo, vcc_lo, 16
	s_mul_i32 s32, vcc_lo, 0xe00
	s_sub_u32 s15, s15, s32
	s_mov_b32 s14, 0
	s_cmp_ge_u32 vcc_lo, 16
	s_cbranch_scc1 .Lcn_dn_n1lf
	s_lshr_b32 s32, s15, 5
	s_mul_i32 s32, s32, 0x2493
	s_lshr_b32 s32, s32, 16
	s_mul_i32 s33, s32, 0xe0
	s_sub_u32 s33, s15, s33
	s_lshl_b32 s32, s32, 2
	s_add_u32 s32, s32, s14
	s_lshr_b32 s15, vcc_lo, 1
	s_and_b32 vcc_lo, vcc_lo, 1
	s_mul_i32 s14, s15, 0x1c00000
	s_add_u32 s14, s14, 0x4a000000
	s_lshr_b32 s15, s33, 2
	s_lshl_b32 s15, s15, 8
	s_lshl_b32 vcc_lo, vcc_lo, 7
	s_add_u32 s15, s15, vcc_lo
	s_and_b32 vcc_lo, s33, 3
	s_lshl_b32 vcc_lo, vcc_lo, 5
	s_add_u32 s15, s15, vcc_lo
	s_lshl_b32 s15, s15, 11
	s_add_u32 s14, s14, s15
	s_lshl_b32 s15, s32, 5
	s_add_u32 s14, s14, s15
	v_readlane_b32 s32, v255, 52
	v_readlane_b32 s33, v255, 53
	s_add_u32 s32, s32, s14
	s_addc_u32 s33, s33, 0
	s_movk_i32 vcc_lo, 0x800
	s_mov_b32 s15, 0x42000000
	s_branch .Lcn_dd_n1lf

; __device__ __forceinline__ unsigned pk4_fp8(float a, float b, float c, float d) { int p = __builtin_amdgcn_cvt_pk_fp8_f32(a, b, 0, false); p = __builtin_amdgcn_cvt_pk_fp8_f32(c, d, p, true); return (unsigned)p; }
; __device__ __forceinline__ void witem_store(const WItem& w, const f32x4 (&v)[16]) {
;     if (!w.valid) return;
;     if (w.f8) {
; #pragma unroll
;         for (int j = 0; j < 4; ++j) { u32x4 o; const float sc = w.scale;
;             o.x = pk4_fp8(v[0][j] * sc, v[1][j] * sc, v[2][j] * sc, v[3][j] * sc); o.y = pk4_fp8(v[4][j] * sc, v[5][j] * sc, v[6][j] * sc, v[7][j] * sc);
;             o.z = pk4_fp8(v[8][j] * sc, v[9][j] * sc, v[10][j] * sc, v[11][j] * sc); o.w = pk4_fp8(v[12][j] * sc, v[13][j] * sc, v[14][j] * sc, v[15][j] * sc);
;             *(u32x4*)(w.dst + (size_t)witem_row(w.kind, w.n + j) * w.K + w.k0) = o; }
; __device__ __forceinline__ void p0_weights(const Args& a, LAS unsigned char* lds) {
;     ...
;     { f32x4 v[16], vn[16];
;       WItem cur = decode(gw); witem_load(cur, v);
; #pragma unroll 1
;       for (int it = gw; it < NIT; it += NGW) {
;           const WItem nxt = decode(it + NGW); witem_load(nxt, vn);
;           __builtin_amdgcn_sched_barrier(0);
;           witem_store(cur, v);
;           __builtin_amdgcn_sched_barrier(0);
; #pragma unroll
;           for (int i = 0; i < 16; ++i) v[i] = vn[i];
;           cur = nxt; } }
.Lcn_dd_n1lf:
	s_lshr_b32 s14, s101, 28
	s_and_b32 s14, s14, 3
	s_and_b32 s15, s67, 3
	s_add_u32 s15, s15, 1
	s_sub_u32 s15, s15, s14
	v_and_b32_e32 v220, 63, v0
	v_lshrrev_b32_e32 v221, 3, v220
	v_and_b32_e32 v220, 7, v220
	v_lshrrev_b32_e32 v253, 1, v220
	v_subrev_u32_e32 v254, s14, v253
	v_cmp_gt_u32_e64 s[14:15], s15, v254
	v_lshrrev_b32_e32 v254, 2, v221
	v_xor_b32_e32 v254, v254, v253
	v_lshlrev_b32_e32 v254, 1, v254
	v_and_b32_e32 v253, 1, v220
	v_or_b32_e32 v254, v254, v253
	v_lshlrev_b32_e32 v254, 4, v254
	v_lshl_add_u32 v254, v221, 7, v254
	v_and_b32_e32 v253, 0x1c0, v0
	v_lshl_add_u32 v254, v253, 6, v254
	v_add_u32_e32 v254, 0x1c000, v254
	v_xor_b32_e32 v253, 64, v254
	v_mul_u32_u24_e32 v221, vcc_lo, v221
	v_lshl_add_u32 v221, v220, 4, v221
	s_mov_b64 exec, s[14:15]
	ds_read_b128 v[212:215], v254
	ds_read_b128 v[216:219], v253 offset:1024
	ds_read_b128 v[224:227], v254 offset:2048
	s_lshl_b32 vcc_lo, vcc_lo, 3
	s_waitcnt lgkmcnt(0)
	global_store_dwordx4 v221, v[212:215], s[32:33] nt
	s_add_u32 s32, s32, vcc_lo
	s_addc_u32 s33, s33, 0
	s_nop 1
	ds_read_b128 v[212:215], v253 offset:3072
	global_store_dwordx4 v221, v[216:219], s[32:33] nt
	s_add_u32 s32, s32, vcc_lo
	s_addc_u32 s33, s33, 0
	global_store_dwordx4 v221, v[224:227], s[32:33] nt
	s_add_u32 s32, s32, vcc_lo
	s_addc_u32 s33, s33, 0
	s_waitcnt lgkmcnt(0)
	global_store_dwordx4 v221, v[212:215], s[32:33] nt
	s_mov_b64 exec, -1
	s_and_b32 vcc_lo, s67, 3
	s_add_u32 vcc_lo, vcc_lo, 1
	s_and_b32 vcc_lo, vcc_lo, 3
	s_lshl_b32 vcc_lo, vcc_lo, 28
	s_andn2_b32 s101, s101, 0x30000000
	s_or_b32 s101, s101, vcc_lo
	s_mov_b32 s67, 0
.Lcn_fnone_n1l:
	s_mov_b32 s25, 0
	s_cmp_gt_i32 s70, s17
	s_cbranch_scc1 .Lcn_lskip_n1l
	s_and_b32 s14, s101, 0xfffffff
	s_cmp_ge_u32 s14, 168
	s_cbranch_scc1 .Lcn_ldum_n1l
	s_and_b32 s14, s101, 0xfffffff
	s_lshr_b32 s15, s14, 2
	s_lshl_b32 s15, s15, 11
	s_add_u32 s15, s15, s100
	s_lshr_b32 vcc_lo, s15, 9
	s_mul_i32 vcc_lo, vcc_lo, 0x2493
	s_lshr_b32 vcc_lo, vcc_lo, 16
	s_mul_i32 s32, vcc_lo, 0xe00
	s_sub_u32 s15, s15, s32
	s_and_b32 s14, s14, 3
	s_cmp_ge_u32 vcc_lo, 16
	s_cbranch_scc1 .Lcn_dn_n1ls
	s_lshr_b32 s32, s15, 5
	s_mul_i32 s32, s32, 0x2493
	s_lshr_b32 s32, s32, 16
	s_mul_i32 s33, s32, 0xe0
	s_sub_u32 s33, s15, s33
	s_lshl_b32 s32, s32, 2
	s_add_u32 s32, s32, s14
	s_lshr_b32 s15, vcc_lo, 1
	s_and_b32 vcc_lo, vcc_lo, 1
	s_mul_i32 s14, s15, 0x3800000
	s_mul_i32 s15, s32, 0xe0000
	s_add_u32 s14, s14, s15
	s_lshl_b32 s15, s33, 7
	s_add_u32 s14, s14, s15
	v_readlane_b32 s32, v255, 46
	v_readlane_b32 s33, v255, 47
	s_cmp_eq_u32 vcc_lo, 0
	s_cselect_b32 s32, s98, s32
	s_cselect_b32 s33, s99, s33
	s_add_u32 s32, s32, s14
	s_addc_u32 s33, s33, 0
	s_movk_i32 vcc_lo, 0x7000
	s_branch .Lcn_dd_n1ls

; __device__ __forceinline__ void witem_load(const WItem& w, f32x4 (&v)[16]) {
;     if (!w.valid) return;
; #pragma unroll
;     for (int i = 0; i < 16; ++i) v[i] = *(const f32x4*)(w.src + (size_t)i * w.N);
; }
.Lcn_lgo_n1l:
	v_and_b32_e32 v220, 63, v0
	v_and_b32_e32 v253, 7, v220
	v_lshrrev_b32_e32 v220, 3, v220
	v_lshlrev_b32_e32 v220, 2, v220
	v_lshlrev_b32_e32 v221, 4, v253
	v_lshlrev_b32_e32 v253, 2, v253
	v_mad_u32_u24 v254, v220, vcc_lo, v221
	global_load_dwordx4 v[212:215], v254, s[32:33] nt
	s_add_u32 s32, s32, vcc_lo
	s_addc_u32 s33, s33, 0
	global_load_dwordx4 v[216:219], v254, s[32:33] nt
	s_add_u32 s32, s32, vcc_lo
	s_addc_u32 s33, s33, 0
	global_load_dwordx4 v[224:227], v254, s[32:33] nt
	s_add_u32 s32, s32, vcc_lo
	s_addc_u32 s33, s33, 0
	global_load_dwordx2 v[220:221], v254, s[32:33] offset:0 nt
	global_load_dword v253, v254, s[32:33] offset:8 nt
	global_load_dword v254, v254, s[32:33] offset:12 nt

; __device__ __forceinline__ unsigned pk4_fp8(float a, float b, float c, float d) { int p = __builtin_amdgcn_cvt_pk_fp8_f32(a, b, 0, false); p = __builtin_amdgcn_cvt_pk_fp8_f32(c, d, p, true); return (unsigned)p; }
; __device__ __forceinline__ void witem_store(const WItem& w, const f32x4 (&v)[16]) {
;     if (!w.valid) return;
;     if (w.f8) {
; #pragma unroll
;         for (int j = 0; j < 4; ++j) { u32x4 o; const float sc = w.scale;
;             o.x = pk4_fp8(v[0][j] * sc, v[1][j] * sc, v[2][j] * sc, v[3][j] * sc); o.y = pk4_fp8(v[4][j] * sc, v[5][j] * sc, v[6][j] * sc, v[7][j] * sc);
;             o.z = pk4_fp8(v[8][j] * sc, v[9][j] * sc, v[10][j] * sc, v[11][j] * sc); o.w = pk4_fp8(v[12][j] * sc, v[13][j] * sc, v[14][j] * sc, v[15][j] * sc);
;             *(u32x4*)(w.dst + (size_t)witem_row(w.kind, w.n + j) * w.K + w.k0) = o; }
; __device__ __forceinline__ void p0_weights(const Args& a, LAS unsigned char* lds) {
;     ...
;         else if ((r -= I_FD) < 16 * I_MG) { const int up = r / (8 * I_MG); r -= up * 8 * I_MG; const int e = r / I_MG; r -= e * I_MG; W = a.in[up ? I_MWU : I_MWG] + (size_t)e * D * DFE; w.K = D; w.N = DFE;
;             w.dst = a.ws + WS_MGU_T + (size_t)e * 2 * DFE * D * (MOE_FP8 ? 1 : 2); w.kind = 2 + up; w.f8 = MOE_FP8; w.scale = F8_WGU; }
;         else { r -= 16 * I_MG; const int e = r / I_MD; r -= e * I_MD; W = a.in[I_MWD] + (size_t)e * DFE * D; w.K = DFE; w.N = D; w.dst = a.ws + WS_MD_T + (size_t)e * D * DFE * (MOE_FP8 ? 1 : 2); w.f8 = MOE_FP8; w.scale = F8_WD; }
;         const int nblk = (w.N + 31) >> 5, kb = r / nblk, nb = r - kb * nblk;
;         w.k0 = 128 * kb + 16 * (lane >> 3); w.n = 32 * nb + 4 * (lane & 7); w.valid = w.n < w.N; w.src = W + (size_t)w.k0 * w.N + w.n;
.Lcn_exit_n1:
	s_bitcmp1_b32 s25, 31
	s_cbranch_scc0 .Lcn_xnone_n1
	s_waitcnt vmcnt(0)
	s_bitcmp1_b32 s25, 31
	s_cbranch_scc0 .Lcn_snone_n1x
	s_and_b32 s14, s25, 0xfffffff
	s_lshr_b32 s15, s14, 2
	s_lshl_b32 s15, s15, 11
	s_add_u32 s15, s15, s100
	s_lshr_b32 vcc_lo, s15, 9
	s_mul_i32 vcc_lo, vcc_lo, 0x2493
	s_lshr_b32 vcc_lo, vcc_lo, 16
	s_mul_i32 s32, vcc_lo, 0xe00
	s_sub_u32 s15, s15, s32
	s_and_b32 s14, s14, 3
	s_cmp_ge_u32 vcc_lo, 16
	s_cbranch_scc1 .Lcn_dn_n1xd
	s_lshr_b32 s32, s15, 5
	s_mul_i32 s32, s32, 0x2493
	s_lshr_b32 s32, s32, 16
	s_mul_i32 s33, s32, 0xe0
	s_sub_u32 s33, s15, s33
	s_lshl_b32 s32, s32, 2
	s_add_u32 s32, s32, s14
	s_lshr_b32 s15, vcc_lo, 1
	s_and_b32 vcc_lo, vcc_lo, 1
	s_mul_i32 s14, s15, 0x1c00000
	s_add_u32 s14, s14, 0x4a000000
	s_lshr_b32 s15, s33, 2
	s_lshl_b32 s15, s15, 8
	s_lshl_b32 vcc_lo, vcc_lo, 7
	s_add_u32 s15, s15, vcc_lo
	s_and_b32 vcc_lo, s33, 3
	s_lshl_b32 vcc_lo, vcc_lo, 5
	s_add_u32 s15, s15, vcc_lo
	s_lshl_b32 s15, s15, 11
	s_add_u32 s14, s14, s15
	s_lshl_b32 s15, s32, 5
	s_add_u32 s14, s14, s15
	v_readlane_b32 s32, v255, 52
	v_readlane_b32 s33, v255, 53
	s_add_u32 s32, s32, s14
	s_addc_u32 s33, s33, 0
	s_movk_i32 vcc_lo, 0x800
	s_mov_b32 s15, 0x42000000
	s_branch .Lcn_dd_n1xd

; __device__ __forceinline__ unsigned pk4_fp8(float a, float b, float c, float d) { int p = __builtin_amdgcn_cvt_pk_fp8_f32(a, b, 0, false); p = __builtin_amdgcn_cvt_pk_fp8_f32(c, d, p, true); return (unsigned)p; }
; __device__ __forceinline__ void witem_store(const WItem& w, const f32x4 (&v)[16]) {
;     if (!w.valid) return;
;     if (w.f8) {
; #pragma unroll
;         for (int j = 0; j < 4; ++j) { u32x4 o; const float sc = w.scale;
;             o.x = pk4_fp8(v[0][j] * sc, v[1][j] * sc, v[2][j] * sc, v[3][j] * sc); o.y = pk4_fp8(v[4][j] * sc, v[5][j] * sc, v[6][j] * sc, v[7][j] * sc);
;             o.z = pk4_fp8(v[8][j] * sc, v[9][j] * sc, v[10][j] * sc, v[11][j] * sc); o.w = pk4_fp8(v[12][j] * sc, v[13][j] * sc, v[14][j] * sc, v[15][j] * sc);
;             *(u32x4*)(w.dst + (size_t)witem_row(w.kind, w.n + j) * w.K + w.k0) = o; }
; __device__ __forceinline__ void p0_weights(const Args& a, LAS unsigned char* lds) {
;     ...
;         else if ((r -= I_FD) < 16 * I_MG) { const int up = r / (8 * I_MG); r -= up * 8 * I_MG; const int e = r / I_MG; r -= e * I_MG; W = a.in[up ? I_MWU : I_MWG] + (size_t)e * D * DFE; w.K = D; w.N = DFE;
;             w.dst = a.ws + WS_MGU_T + (size_t)e * 2 * DFE * D * (MOE_FP8 ? 1 : 2); w.kind = 2 + up; w.f8 = MOE_FP8; w.scale = F8_WGU; }
;         else { r -= 16 * I_MG; const int e = r / I_MD; r -= e * I_MD; W = a.in[I_MWD] + (size_t)e * DFE * D; w.K = DFE; w.N = D; w.dst = a.ws + WS_MD_T + (size_t)e * D * DFE * (MOE_FP8 ? 1 : 2); w.f8 = MOE_FP8; w.scale = F8_WD; }
;         const int nblk = (w.N + 31) >> 5, kb = r / nblk, nb = r - kb * nblk;
;         w.k0 = 128 * kb + 16 * (lane >> 3); w.n = 32 * nb + 4 * (lane & 7); w.valid = w.n < w.N; w.src = W + (size_t)w.k0 * w.N + w.n;
.Lcn_snone_n1x:
.Lcn_xnone_n1:
	s_bitcmp1_b32 s67, 31
	s_cbranch_scc0 .Lcn_fnone_n1x
	s_and_b32 s14, s67, 0xfffffff
	s_lshr_b32 s15, s14, 2
	s_lshl_b32 s15, s15, 11
	s_add_u32 s15, s15, s100
	s_lshr_b32 vcc_lo, s15, 9
	s_mul_i32 vcc_lo, vcc_lo, 0x2493
	s_lshr_b32 vcc_lo, vcc_lo, 16
	s_mul_i32 s32, vcc_lo, 0xe00
	s_sub_u32 s15, s15, s32
	s_mov_b32 s14, 0
	s_cmp_ge_u32 vcc_lo, 16
	s_cbranch_scc1 .Lcn_dn_n1xf
	s_lshr_b32 s32, s15, 5
	s_mul_i32 s32, s32, 0x2493
	s_lshr_b32 s32, s32, 16
	s_mul_i32 s33, s32, 0xe0
	s_sub_u32 s33, s15, s33
	s_lshl_b32 s32, s32, 2
	s_add_u32 s32, s32, s14
	s_lshr_b32 s15, vcc_lo, 1
	s_and_b32 vcc_lo, vcc_lo, 1
	s_mul_i32 s14, s15, 0x1c00000
	s_add_u32 s14, s14, 0x4a000000
	s_lshr_b32 s15, s33, 2
	s_lshl_b32 s15, s15, 8
	s_lshl_b32 vcc_lo, vcc_lo, 7
	s_add_u32 s15, s15, vcc_lo
	s_and_b32 vcc_lo, s33, 3
	s_lshl_b32 vcc_lo, vcc_lo, 5
	s_add_u32 s15, s15, vcc_lo
	s_lshl_b32 s15, s15, 11
	s_add_u32 s14, s14, s15
	s_lshl_b32 s15, s32, 5
	s_add_u32 s14, s14, s15
	v_readlane_b32 s32, v255, 52
	v_readlane_b32 s33, v255, 53
	s_add_u32 s32, s32, s14
	s_addc_u32 s33, s33, 0
	s_movk_i32 vcc_lo, 0x800
	s_mov_b32 s15, 0x42000000
	s_branch .Lcn_dd_n1xf

; __device__ __forceinline__ void p0_weights(const Args& a, LAS unsigned char* lds) {
;     ...
;         else if ((r -= I_FD) < 16 * I_MG) { const int up = r / (8 * I_MG); r -= up * 8 * I_MG; const int e = r / I_MG; r -= e * I_MG; W = a.in[up ? I_MWU : I_MWG] + (size_t)e * D * DFE; w.K = D; w.N = DFE;
;             w.dst = a.ws + WS_MGU_T + (size_t)e * 2 * DFE * D * (MOE_FP8 ? 1 : 2); w.kind = 2 + up; w.f8 = MOE_FP8; w.scale = F8_WGU; }
;         else { r -= 16 * I_MG; const int e = r / I_MD; r -= e * I_MD; W = a.in[I_MWD] + (size_t)e * DFE * D; w.K = DFE; w.N = D; w.dst = a.ws + WS_MD_T + (size_t)e * D * DFE * (MOE_FP8 ? 1 : 2); w.f8 = MOE_FP8; w.scale = F8_WD; }
;         const int nblk = (w.N + 31) >> 5, kb = r / nblk, nb = r - kb * nblk;
;         w.k0 = 128 * kb + 16 * (lane >> 3); w.n = 32 * nb + 4 * (lane & 7); w.valid = w.n < w.N; w.src = W + (size_t)w.k0 * w.N + w.n;
.LBB0_1880:
.Lcn_left:
	s_and_b32 s8, s101, 0xfffffff
	s_cmp_ge_u32 s8, 168
	s_cbranch_scc1 .Lcn_leftdone
	s_and_b32 s8, s101, 0xfffffff
	s_cmp_ge_u32 s8, 168
	s_cbranch_scc1 .Lcn_ldum_lfA
	s_and_b32 s8, s101, 0xfffffff
	s_lshr_b32 s9, s8, 2
	s_lshl_b32 s9, s9, 11
	s_add_u32 s9, s9, s100
	s_lshr_b32 s10, s9, 9
	s_mul_i32 s10, s10, 0x2493
	s_lshr_b32 s10, s10, 16
	s_mul_i32 s32, s10, 0xe00
	s_sub_u32 s9, s9, s32
	s_and_b32 s8, s8, 3
	s_cmp_ge_u32 s10, 16
	s_cbranch_scc1 .Lcn_dn_lfAs
	s_lshr_b32 s32, s9, 5
	s_mul_i32 s32, s32, 0x2493
	s_lshr_b32 s32, s32, 16
	s_mul_i32 s33, s32, 0xe0
	s_sub_u32 s33, s9, s33
	s_lshl_b32 s32, s32, 2
	s_add_u32 s32, s32, s8
	s_lshr_b32 s9, s10, 1
	s_and_b32 s10, s10, 1
	s_mul_i32 s8, s9, 0x3800000
	s_mul_i32 s9, s32, 0xe0000
	s_add_u32 s8, s8, s9
	s_lshl_b32 s9, s33, 7
	s_add_u32 s8, s8, s9
	v_readlane_b32 s32, v255, 46
	v_readlane_b32 s33, v255, 47
	s_cmp_eq_u32 s10, 0
	s_cselect_b32 s32, s98, s32
	s_cselect_b32 s33, s99, s33
	s_add_u32 s32, s32, s8
	s_addc_u32 s33, s33, 0
	s_movk_i32 s10, 0x7000
	s_branch .Lcn_dd_lfAs
.Lcn_dn_lfAs:
	s_lshr_b32 s32, s9, 6
	s_and_b32 s33, s9, 63
	s_lshl_b32 s32, s32, 2
	s_add_u32 s32, s32, s8
	s_sub_u32 s9, s10, 16
	s_mul_i32 s8, s9, 0x3800000
	s_lshl_b32 s9, s32, 18
	s_add_u32 s8, s8, s9
	s_lshl_b32 s9, s33, 7
	s_add_u32 s8, s8, s9
	v_readlane_b32 s32, v255, 48
	v_readlane_b32 s33, v255, 49
	s_add_u32 s32, s32, s8
	s_addc_u32 s33, s33, 0
	s_movk_i32 s10, 0x2000

; __device__ __forceinline__ void witem_load(const WItem& w, f32x4 (&v)[16]) {
;     if (!w.valid) return;
; #pragma unroll
;     for (int i = 0; i < 16; ++i) v[i] = *(const f32x4*)(w.src + (size_t)i * w.N);
; }
; __device__ __forceinline__ void p0_weights(const Args& a, LAS unsigned char* lds) {
;     ...
;         else if ((r -= I_FD) < 16 * I_MG) { const int up = r / (8 * I_MG); r -= up * 8 * I_MG; const int e = r / I_MG; r -= e * I_MG; W = a.in[up ? I_MWU : I_MWG] + (size_t)e * D * DFE; w.K = D; w.N = DFE;
;             w.dst = a.ws + WS_MGU_T + (size_t)e * 2 * DFE * D * (MOE_FP8 ? 1 : 2); w.kind = 2 + up; w.f8 = MOE_FP8; w.scale = F8_WGU; }
;         else { r -= 16 * I_MG; const int e = r / I_MD; r -= e * I_MD; W = a.in[I_MWD] + (size_t)e * DFE * D; w.K = DFE; w.N = D; w.dst = a.ws + WS_MD_T + (size_t)e * D * DFE * (MOE_FP8 ? 1 : 2); w.f8 = MOE_FP8; w.scale = F8_WD; }
;         const int nblk = (w.N + 31) >> 5, kb = r / nblk, nb = r - kb * nblk;
;         w.k0 = 128 * kb + 16 * (lane >> 3); w.n = 32 * nb + 4 * (lane & 7); w.valid = w.n < w.N; w.src = W + (size_t)w.k0 * w.N + w.n;
.Lcn_ldum_lfA:
	v_readlane_b32 s32, v255, 52
	v_readlane_b32 s33, v255, 53
	s_add_u32 s32, s32, 0x500000
	s_addc_u32 s33, s33, 0
	s_movk_i32 s10, 0x2000
	s_mov_b32 s25, 0
.Lcn_lgo_lfA:
	v_and_b32_e32 v112, 63, v0
	v_and_b32_e32 v114, 7, v112
	v_lshrrev_b32_e32 v112, 3, v112
	v_lshlrev_b32_e32 v112, 2, v112
	v_lshlrev_b32_e32 v113, 4, v114
	v_lshlrev_b32_e32 v114, 2, v114
	v_mad_u32_u24 v115, v112, s10, v113
	global_load_dwordx4 v[100:103], v115, s[32:33] nt
	s_add_u32 s32, s32, s10
	s_addc_u32 s33, s33, 0
	global_load_dwordx4 v[104:107], v115, s[32:33] nt
	s_add_u32 s32, s32, s10
	s_addc_u32 s33, s33, 0
	global_load_dwordx4 v[108:111], v115, s[32:33] nt
	s_add_u32 s32, s32, s10
	s_addc_u32 s33, s33, 0
	global_load_dwordx4 v[112:115], v115, s[32:33] nt
	s_and_b32 s8, s101, 0xfffffff
	s_cmp_ge_u32 s8, 168
	s_cbranch_scc1 .Lcn_ldum_lfB
	s_and_b32 s8, s101, 0xfffffff
	s_lshr_b32 s9, s8, 2
	s_lshl_b32 s9, s9, 11
	s_add_u32 s9, s9, s100
	s_lshr_b32 s10, s9, 9
	s_mul_i32 s10, s10, 0x2493
	s_lshr_b32 s10, s10, 16
	s_mul_i32 s32, s10, 0xe00
	s_sub_u32 s9, s9, s32
	s_and_b32 s8, s8, 3
	s_cmp_ge_u32 s10, 16
	s_cbranch_scc1 .Lcn_dn_lfBs
	s_lshr_b32 s32, s9, 5
	s_mul_i32 s32, s32, 0x2493
	s_lshr_b32 s32, s32, 16
	s_mul_i32 s33, s32, 0xe0
	s_sub_u32 s33, s9, s33
	s_lshl_b32 s32, s32, 2
	s_add_u32 s32, s32, s8
	s_lshr_b32 s9, s10, 1
	s_and_b32 s10, s10, 1
	s_mul_i32 s8, s9, 0x3800000
	s_mul_i32 s9, s32, 0xe0000
	s_add_u32 s8, s8, s9
	s_lshl_b32 s9, s33, 7
	s_add_u32 s8, s8, s9
	v_readlane_b32 s32, v255, 46
	v_readlane_b32 s33, v255, 47
	s_cmp_eq_u32 s10, 0
	s_cselect_b32 s32, s98, s32
	s_cselect_b32 s33, s99, s33
	s_add_u32 s32, s32, s8
	s_addc_u32 s33, s33, 0
	s_movk_i32 s10, 0x7000
	s_branch .Lcn_dd_lfBs

; __device__ __forceinline__ void witem_load(const WItem& w, f32x4 (&v)[16]) {
;     if (!w.valid) return;
; #pragma unroll
;     for (int i = 0; i < 16; ++i) v[i] = *(const f32x4*)(w.src + (size_t)i * w.N);
; }
; __device__ __forceinline__ void p0_weights(const Args& a, LAS unsigned char* lds) {
;     ...
;         else if ((r -= I_FD) < 16 * I_MG) { const int up = r / (8 * I_MG); r -= up * 8 * I_MG; const int e = r / I_MG; r -= e * I_MG; W = a.in[up ? I_MWU : I_MWG] + (size_t)e * D * DFE; w.K = D; w.N = DFE;
;             w.dst = a.ws + WS_MGU_T + (size_t)e * 2 * DFE * D * (MOE_FP8 ? 1 : 2); w.kind = 2 + up; w.f8 = MOE_FP8; w.scale = F8_WGU; }
;         else { r -= 16 * I_MG; const int e = r / I_MD; r -= e * I_MD; W = a.in[I_MWD] + (size_t)e * DFE * D; w.K = DFE; w.N = D; w.dst = a.ws + WS_MD_T + (size_t)e * D * DFE * (MOE_FP8 ? 1 : 2); w.f8 = MOE_FP8; w.scale = F8_WD; }
;         const int nblk = (w.N + 31) >> 5, kb = r / nblk, nb = r - kb * nblk;
;         w.k0 = 128 * kb + 16 * (lane >> 3); w.n = 32 * nb + 4 * (lane & 7); w.valid = w.n < w.N; w.src = W + (size_t)w.k0 * w.N + w.n;
.Lcn_ldum_lfB:
	v_readlane_b32 s32, v255, 52
	v_readlane_b32 s33, v255, 53
	s_add_u32 s32, s32, 0x500000
	s_addc_u32 s33, s33, 0
	s_movk_i32 s10, 0x2000
	s_mov_b32 s26, 0
.Lcn_lgo_lfB:
	v_and_b32_e32 v128, 63, v0
	v_and_b32_e32 v130, 7, v128
	v_lshrrev_b32_e32 v128, 3, v128
	v_lshlrev_b32_e32 v128, 2, v128
	v_lshlrev_b32_e32 v129, 4, v130
	v_lshlrev_b32_e32 v130, 2, v130
	v_mad_u32_u24 v131, v128, s10, v129
	global_load_dwordx4 v[116:119], v131, s[32:33] nt
	s_add_u32 s32, s32, s10
	s_addc_u32 s33, s33, 0
	global_load_dwordx4 v[120:123], v131, s[32:33] nt
	s_add_u32 s32, s32, s10
	s_addc_u32 s33, s33, 0
	global_load_dwordx4 v[124:127], v131, s[32:33] nt
	s_add_u32 s32, s32, s10
	s_addc_u32 s33, s33, 0
	global_load_dwordx4 v[128:131], v131, s[32:33] nt
	s_and_b32 s8, s101, 0xfffffff
	s_cmp_ge_u32 s8, 168
	s_cbranch_scc1 .Lcn_ldum_lfC
	s_and_b32 s8, s101, 0xfffffff
	s_lshr_b32 s9, s8, 2
	s_lshl_b32 s9, s9, 11
	s_add_u32 s9, s9, s100
	s_lshr_b32 s10, s9, 9
	s_mul_i32 s10, s10, 0x2493
	s_lshr_b32 s10, s10, 16
	s_mul_i32 s32, s10, 0xe00
	s_sub_u32 s9, s9, s32
	s_and_b32 s8, s8, 3
	s_cmp_ge_u32 s10, 16
	s_cbranch_scc1 .Lcn_dn_lfCs
	s_lshr_b32 s32, s9, 5
	s_mul_i32 s32, s32, 0x2493
	s_lshr_b32 s32, s32, 16
	s_mul_i32 s33, s32, 0xe0
	s_sub_u32 s33, s9, s33
	s_lshl_b32 s32, s32, 2
	s_add_u32 s32, s32, s8
	s_lshr_b32 s9, s10, 1
	s_and_b32 s10, s10, 1
	s_mul_i32 s8, s9, 0x3800000
	s_mul_i32 s9, s32, 0xe0000
	s_add_u32 s8, s8, s9
	s_lshl_b32 s9, s33, 7
	s_add_u32 s8, s8, s9
	v_readlane_b32 s32, v255, 46
	v_readlane_b32 s33, v255, 47
	s_cmp_eq_u32 s10, 0
	s_cselect_b32 s32, s98, s32
	s_cselect_b32 s33, s99, s33
	s_add_u32 s32, s32, s8
	s_addc_u32 s33, s33, 0
	s_movk_i32 s10, 0x7000
	s_branch .Lcn_dd_lfCs

; __device__ __forceinline__ void witem_load(const WItem& w, f32x4 (&v)[16]) {
;     if (!w.valid) return;
; #pragma unroll
;     for (int i = 0; i < 16; ++i) v[i] = *(const f32x4*)(w.src + (size_t)i * w.N);
; }
; __device__ __forceinline__ void p0_weights(const Args& a, LAS unsigned char* lds) {
;     ...
;         else if ((r -= I_FD) < 16 * I_MG) { const int up = r / (8 * I_MG); r -= up * 8 * I_MG; const int e = r / I_MG; r -= e * I_MG; W = a.in[up ? I_MWU : I_MWG] + (size_t)e * D * DFE; w.K = D; w.N = DFE;
;             w.dst = a.ws + WS_MGU_T + (size_t)e * 2 * DFE * D * (MOE_FP8 ? 1 : 2); w.kind = 2 + up; w.f8 = MOE_FP8; w.scale = F8_WGU; }
;         else { r -= 16 * I_MG; const int e = r / I_MD; r -= e * I_MD; W = a.in[I_MWD] + (size_t)e * DFE * D; w.K = DFE; w.N = D; w.dst = a.ws + WS_MD_T + (size_t)e * D * DFE * (MOE_FP8 ? 1 : 2); w.f8 = MOE_FP8; w.scale = F8_WD; }
;         const int nblk = (w.N + 31) >> 5, kb = r / nblk, nb = r - kb * nblk;
;         w.k0 = 128 * kb + 16 * (lane >> 3); w.n = 32 * nb + 4 * (lane & 7); w.valid = w.n < w.N; w.src = W + (size_t)w.k0 * w.N + w.n;
.Lcn_ldum_lfC:
	v_readlane_b32 s32, v255, 52
	v_readlane_b32 s33, v255, 53
	s_add_u32 s32, s32, 0x500000
	s_addc_u32 s33, s33, 0
	s_movk_i32 s10, 0x2000
	s_mov_b32 s27, 0
.Lcn_lgo_lfC:
	v_and_b32_e32 v144, 63, v0
	v_and_b32_e32 v146, 7, v144
	v_lshrrev_b32_e32 v144, 3, v144
	v_lshlrev_b32_e32 v144, 2, v144
	v_lshlrev_b32_e32 v145, 4, v146
	v_lshlrev_b32_e32 v146, 2, v146
	v_mad_u32_u24 v147, v144, s10, v145
	global_load_dwordx4 v[132:135], v147, s[32:33] nt
	s_add_u32 s32, s32, s10
	s_addc_u32 s33, s33, 0
	global_load_dwordx4 v[136:139], v147, s[32:33] nt
	s_add_u32 s32, s32, s10
	s_addc_u32 s33, s33, 0
	global_load_dwordx4 v[140:143], v147, s[32:33] nt
	s_add_u32 s32, s32, s10
	s_addc_u32 s33, s33, 0
	global_load_dwordx4 v[144:147], v147, s[32:33] nt
	s_and_b32 s8, s101, 0xfffffff
	s_cmp_ge_u32 s8, 168
	s_cbranch_scc1 .Lcn_ldum_lfD
	s_and_b32 s8, s101, 0xfffffff
	s_lshr_b32 s9, s8, 2
	s_lshl_b32 s9, s9, 11
	s_add_u32 s9, s9, s100
	s_lshr_b32 s10, s9, 9
	s_mul_i32 s10, s10, 0x2493
	s_lshr_b32 s10, s10, 16
	s_mul_i32 s32, s10, 0xe00
	s_sub_u32 s9, s9, s32
	s_and_b32 s8, s8, 3
	s_cmp_ge_u32 s10, 16
	s_cbranch_scc1 .Lcn_dn_lfDs
	s_lshr_b32 s32, s9, 5
	s_mul_i32 s32, s32, 0x2493
	s_lshr_b32 s32, s32, 16
	s_mul_i32 s33, s32, 0xe0
	s_sub_u32 s33, s9, s33
	s_lshl_b32 s32, s32, 2
	s_add_u32 s32, s32, s8
	s_lshr_b32 s9, s10, 1
	s_and_b32 s10, s10, 1
	s_mul_i32 s8, s9, 0x3800000
	s_mul_i32 s9, s32, 0xe0000
	s_add_u32 s8, s8, s9
	s_lshl_b32 s9, s33, 7
	s_add_u32 s8, s8, s9
	v_readlane_b32 s32, v255, 46
	v_readlane_b32 s33, v255, 47
	s_cmp_eq_u32 s10, 0
	s_cselect_b32 s32, s98, s32
	s_cselect_b32 s33, s99, s33
	s_add_u32 s32, s32, s8
	s_addc_u32 s33, s33, 0
	s_movk_i32 s10, 0x7000
	s_branch .Lcn_dd_lfDs

; __device__ __forceinline__ unsigned pk4_fp8(float a, float b, float c, float d) { int p = __builtin_amdgcn_cvt_pk_fp8_f32(a, b, 0, false); p = __builtin_amdgcn_cvt_pk_fp8_f32(c, d, p, true); return (unsigned)p; }
; __device__ __forceinline__ void witem_store(const WItem& w, const f32x4 (&v)[16]) {
;     if (!w.valid) return;
;     if (w.f8) {
; #pragma unroll
;         for (int j = 0; j < 4; ++j) { u32x4 o; const float sc = w.scale;
;             o.x = pk4_fp8(v[0][j] * sc, v[1][j] * sc, v[2][j] * sc, v[3][j] * sc); o.y = pk4_fp8(v[4][j] * sc, v[5][j] * sc, v[6][j] * sc, v[7][j] * sc);
;             o.z = pk4_fp8(v[8][j] * sc, v[9][j] * sc, v[10][j] * sc, v[11][j] * sc); o.w = pk4_fp8(v[12][j] * sc, v[13][j] * sc, v[14][j] * sc, v[15][j] * sc);
;             *(u32x4*)(w.dst + (size_t)witem_row(w.kind, w.n + j) * w.K + w.k0) = o; }
; __device__ __forceinline__ void p0_weights(const Args& a, LAS unsigned char* lds) {
;     ...
;         else if ((r -= I_FD) < 16 * I_MG) { const int up = r / (8 * I_MG); r -= up * 8 * I_MG; const int e = r / I_MG; r -= e * I_MG; W = a.in[up ? I_MWU : I_MWG] + (size_t)e * D * DFE; w.K = D; w.N = DFE;
;             w.dst = a.ws + WS_MGU_T + (size_t)e * 2 * DFE * D * (MOE_FP8 ? 1 : 2); w.kind = 2 + up; w.f8 = MOE_FP8; w.scale = F8_WGU; }
;         else { r -= 16 * I_MG; const int e = r / I_MD; r -= e * I_MD; W = a.in[I_MWD] + (size_t)e * DFE * D; w.K = DFE; w.N = D; w.dst = a.ws + WS_MD_T + (size_t)e * D * DFE * (MOE_FP8 ? 1 : 2); w.f8 = MOE_FP8; w.scale = F8_WD; }
;         const int nblk = (w.N + 31) >> 5, kb = r / nblk, nb = r - kb * nblk;
;         w.k0 = 128 * kb + 16 * (lane >> 3); w.n = 32 * nb + 4 * (lane & 7); w.valid = w.n < w.N; w.src = W + (size_t)w.k0 * w.N + w.n;
.Lcn_ldum_lfD:
	v_readlane_b32 s32, v255, 52
	v_readlane_b32 s33, v255, 53
	s_add_u32 s32, s32, 0x500000
	s_addc_u32 s33, s33, 0
	s_movk_i32 s10, 0x2000
	s_mov_b32 s28, 0
.Lcn_lgo_lfD:
	v_and_b32_e32 v160, 63, v0
	v_and_b32_e32 v162, 7, v160
	v_lshrrev_b32_e32 v160, 3, v160
	v_lshlrev_b32_e32 v160, 2, v160
	v_lshlrev_b32_e32 v161, 4, v162
	v_lshlrev_b32_e32 v162, 2, v162
	v_mad_u32_u24 v163, v160, s10, v161
	global_load_dwordx4 v[148:151], v163, s[32:33] nt
	s_add_u32 s32, s32, s10
	s_addc_u32 s33, s33, 0
	global_load_dwordx4 v[152:155], v163, s[32:33] nt
	s_add_u32 s32, s32, s10
	s_addc_u32 s33, s33, 0
	global_load_dwordx4 v[156:159], v163, s[32:33] nt
	s_add_u32 s32, s32, s10
	s_addc_u32 s33, s33, 0
	global_load_dwordx4 v[160:163], v163, s[32:33] nt
	s_waitcnt vmcnt(0)
	s_bitcmp1_b32 s25, 31
	s_cbranch_scc0 .Lcn_snone_lfA
	s_and_b32 s8, s25, 0xfffffff
	s_lshr_b32 s9, s8, 2
	s_lshl_b32 s9, s9, 11
	s_add_u32 s9, s9, s100
	s_lshr_b32 s10, s9, 9
	s_mul_i32 s10, s10, 0x2493
	s_lshr_b32 s10, s10, 16
	s_mul_i32 s32, s10, 0xe00
	s_sub_u32 s9, s9, s32
	s_and_b32 s8, s8, 3
	s_cmp_ge_u32 s10, 16
	s_cbranch_scc1 .Lcn_dn_lfAd
	s_lshr_b32 s32, s9, 5
	s_mul_i32 s32, s32, 0x2493
	s_lshr_b32 s32, s32, 16
	s_mul_i32 s33, s32, 0xe0
	s_sub_u32 s33, s9, s33
	s_lshl_b32 s32, s32, 2
	s_add_u32 s32, s32, s8
	s_lshr_b32 s9, s10, 1
	s_and_b32 s10, s10, 1
	s_mul_i32 s8, s9, 0x1c00000
	s_add_u32 s8, s8, 0x4a000000
	s_lshr_b32 s9, s33, 2
	s_lshl_b32 s9, s9, 8
	s_lshl_b32 s10, s10, 7
	s_add_u32 s9, s9, s10
	s_and_b32 s10, s33, 3
	s_lshl_b32 s10, s10, 5
	s_add_u32 s9, s9, s10
	s_lshl_b32 s9, s9, 11
	s_add_u32 s8, s8, s9
	s_lshl_b32 s9, s32, 5
	s_add_u32 s8, s8, s9
	v_readlane_b32 s32, v255, 52
	v_readlane_b32 s33, v255, 53
	s_add_u32 s32, s32, s8
	s_addc_u32 s33, s33, 0
	s_movk_i32 s10, 0x800
	s_mov_b32 s9, 0x42000000
	s_branch .Lcn_dd_lfAd
.Lcn_dn_lfAd:
	s_lshr_b32 s32, s9, 6
	s_and_b32 s33, s9, 63
	s_lshl_b32 s32, s32, 2
	s_add_u32 s32, s32, s8
	s_sub_u32 s9, s10, 16
	s_mul_i32 s8, s9, 0xe00000
	s_add_u32 s8, s8, 0x66000000
	s_mul_i32 s9, s33, 0x38000
	s_add_u32 s8, s8, s9
	s_lshl_b32 s9, s32, 5
	s_add_u32 s8, s8, s9
	v_readlane_b32 s32, v255, 52
	v_readlane_b32 s33, v255, 53
	s_add_u32 s32, s32, s8
	s_addc_u32 s33, s33, 0
	s_movk_i32 s10, 0x1c00
	s_mov_b32 s9, 0x43000000
.Lcn_dd_lfAd:
	s_mov_b32 s25, 0
	v_mul_f32_e32 v100, s9, v100
	v_mul_f32_e32 v101, s9, v101
	v_mul_f32_e32 v102, s9, v102
	v_mul_f32_e32 v103, s9, v103
	v_mul_f32_e32 v104, s9, v104
	v_mul_f32_e32 v105, s9, v105
	v_mul_f32_e32 v106, s9, v106
	v_mul_f32_e32 v107, s9, v107
	v_mul_f32_e32 v108, s9, v108
	v_mul_f32_e32 v109, s9, v109
	v_mul_f32_e32 v110, s9, v110
	v_mul_f32_e32 v111, s9, v111
	v_mul_f32_e32 v112, s9, v112
	v_mul_f32_e32 v113, s9, v113
	v_mul_f32_e32 v114, s9, v114
	v_mul_f32_e32 v115, s9, v115
	v_cvt_pk_fp8_f32 v100, v100, v104
	v_cvt_pk_fp8_f32 v101, v101, v105
	v_cvt_pk_fp8_f32 v102, v102, v106
	v_cvt_pk_fp8_f32 v103, v103, v107
	v_cvt_pk_fp8_f32 v100, v108, v112 op_sel:[0,0,1]
	v_cvt_pk_fp8_f32 v101, v109, v113 op_sel:[0,0,1]
	v_cvt_pk_fp8_f32 v102, v110, v114 op_sel:[0,0,1]
	v_cvt_pk_fp8_f32 v103, v111, v115 op_sel:[0,0,1]
	v_and_b32_e32 v104, 63, v0
	v_and_b32_e32 v106, 7, v104
	v_lshrrev_b32_e32 v104, 3, v104
	v_lshlrev_b32_e32 v104, 2, v104
	v_lshlrev_b32_e32 v105, 4, v106
	v_lshlrev_b32_e32 v106, 2, v106
	v_mad_u32_u24 v105, v106, s10, v104
	global_store_dword v105, v100, s[32:33] nt
	v_add_u32_e32 v104, s10, v105
	global_store_dword v104, v101, s[32:33] nt
	v_add_u32_e32 v106, s10, v104
	global_store_dword v106, v102, s[32:33] nt
	v_add_u32_e32 v107, s10, v106
	global_store_dword v107, v103, s[32:33] nt
.Lcn_snone_lfA:
	s_bitcmp1_b32 s26, 31
	s_cbranch_scc0 .Lcn_snone_lfB
	s_and_b32 s8, s26, 0xfffffff
	s_lshr_b32 s9, s8, 2
	s_lshl_b32 s9, s9, 11
	s_add_u32 s9, s9, s100
	s_lshr_b32 s10, s9, 9
	s_mul_i32 s10, s10, 0x2493
	s_lshr_b32 s10, s10, 16
	s_mul_i32 s32, s10, 0xe00
	s_sub_u32 s9, s9, s32
	s_and_b32 s8, s8, 3
	s_cmp_ge_u32 s10, 16
	s_cbranch_scc1 .Lcn_dn_lfBd
	s_lshr_b32 s32, s9, 5
	s_mul_i32 s32, s32, 0x2493
	s_lshr_b32 s32, s32, 16
	s_mul_i32 s33, s32, 0xe0
	s_sub_u32 s33, s9, s33
	s_lshl_b32 s32, s32, 2
	s_add_u32 s32, s32, s8
	s_lshr_b32 s9, s10, 1
	s_and_b32 s10, s10, 1
	s_mul_i32 s8, s9, 0x1c00000
	s_add_u32 s8, s8, 0x4a000000
	s_lshr_b32 s9, s33, 2
	s_lshl_b32 s9, s9, 8
	s_lshl_b32 s10, s10, 7
	s_add_u32 s9, s9, s10
	s_and_b32 s10, s33, 3
	s_lshl_b32 s10, s10, 5
	s_add_u32 s9, s9, s10
	s_lshl_b32 s9, s9, 11
	s_add_u32 s8, s8, s9
	s_lshl_b32 s9, s32, 5
	s_add_u32 s8, s8, s9
	v_readlane_b32 s32, v255, 52
	v_readlane_b32 s33, v255, 53
	s_add_u32 s32, s32, s8
	s_addc_u32 s33, s33, 0
	s_movk_i32 s10, 0x800
	s_mov_b32 s9, 0x42000000
	s_branch .Lcn_dd_lfBd

; __device__ __forceinline__ unsigned pk4_fp8(float a, float b, float c, float d) { int p = __builtin_amdgcn_cvt_pk_fp8_f32(a, b, 0, false); p = __builtin_amdgcn_cvt_pk_fp8_f32(c, d, p, true); return (unsigned)p; }
; __device__ __forceinline__ void witem_store(const WItem& w, const f32x4 (&v)[16]) {
;     if (!w.valid) return;
;     if (w.f8) {
; #pragma unroll
;         for (int j = 0; j < 4; ++j) { u32x4 o; const float sc = w.scale;
;             o.x = pk4_fp8(v[0][j] * sc, v[1][j] * sc, v[2][j] * sc, v[3][j] * sc); o.y = pk4_fp8(v[4][j] * sc, v[5][j] * sc, v[6][j] * sc, v[7][j] * sc);
;             o.z = pk4_fp8(v[8][j] * sc, v[9][j] * sc, v[10][j] * sc, v[11][j] * sc); o.w = pk4_fp8(v[12][j] * sc, v[13][j] * sc, v[14][j] * sc, v[15][j] * sc);
;             *(u32x4*)(w.dst + (size_t)witem_row(w.kind, w.n + j) * w.K + w.k0) = o; }
; __device__ __forceinline__ void p0_weights(const Args& a, LAS unsigned char* lds) {
;     ...
;         else if ((r -= I_FD) < 16 * I_MG) { const int up = r / (8 * I_MG); r -= up * 8 * I_MG; const int e = r / I_MG; r -= e * I_MG; W = a.in[up ? I_MWU : I_MWG] + (size_t)e * D * DFE; w.K = D; w.N = DFE;
;             w.dst = a.ws + WS_MGU_T + (size_t)e * 2 * DFE * D * (MOE_FP8 ? 1 : 2); w.kind = 2 + up; w.f8 = MOE_FP8; w.scale = F8_WGU; }
;         else { r -= 16 * I_MG; const int e = r / I_MD; r -= e * I_MD; W = a.in[I_MWD] + (size_t)e * DFE * D; w.K = DFE; w.N = D; w.dst = a.ws + WS_MD_T + (size_t)e * D * DFE * (MOE_FP8 ? 1 : 2); w.f8 = MOE_FP8; w.scale = F8_WD; }
;         const int nblk = (w.N + 31) >> 5, kb = r / nblk, nb = r - kb * nblk;
;         w.k0 = 128 * kb + 16 * (lane >> 3); w.n = 32 * nb + 4 * (lane & 7); w.valid = w.n < w.N; w.src = W + (size_t)w.k0 * w.N + w.n;
.Lcn_dd_lfBd:
	s_mov_b32 s26, 0
	v_mul_f32_e32 v116, s9, v116
	v_mul_f32_e32 v117, s9, v117
	v_mul_f32_e32 v118, s9, v118
	v_mul_f32_e32 v119, s9, v119
	v_mul_f32_e32 v120, s9, v120
	v_mul_f32_e32 v121, s9, v121
	v_mul_f32_e32 v122, s9, v122
	v_mul_f32_e32 v123, s9, v123
	v_mul_f32_e32 v124, s9, v124
	v_mul_f32_e32 v125, s9, v125
	v_mul_f32_e32 v126, s9, v126
	v_mul_f32_e32 v127, s9, v127
	v_mul_f32_e32 v128, s9, v128
	v_mul_f32_e32 v129, s9, v129
	v_mul_f32_e32 v130, s9, v130
	v_mul_f32_e32 v131, s9, v131
	v_cvt_pk_fp8_f32 v116, v116, v120
	v_cvt_pk_fp8_f32 v117, v117, v121
	v_cvt_pk_fp8_f32 v118, v118, v122
	v_cvt_pk_fp8_f32 v119, v119, v123
	v_cvt_pk_fp8_f32 v116, v124, v128 op_sel:[0,0,1]
	v_cvt_pk_fp8_f32 v117, v125, v129 op_sel:[0,0,1]
	v_cvt_pk_fp8_f32 v118, v126, v130 op_sel:[0,0,1]
	v_cvt_pk_fp8_f32 v119, v127, v131 op_sel:[0,0,1]
	v_and_b32_e32 v120, 63, v0
	v_and_b32_e32 v122, 7, v120
	v_lshrrev_b32_e32 v120, 3, v120
	v_lshlrev_b32_e32 v120, 2, v120
	v_lshlrev_b32_e32 v121, 4, v122
	v_lshlrev_b32_e32 v122, 2, v122
	v_mad_u32_u24 v121, v122, s10, v120
	global_store_dword v121, v116, s[32:33] nt
	v_add_u32_e32 v120, s10, v121
	global_store_dword v120, v117, s[32:33] nt
	v_add_u32_e32 v122, s10, v120
	global_store_dword v122, v118, s[32:33] nt
	v_add_u32_e32 v123, s10, v122
	global_store_dword v123, v119, s[32:33] nt
.Lcn_snone_lfB:
	s_bitcmp1_b32 s27, 31
	s_cbranch_scc0 .Lcn_snone_lfC
	s_and_b32 s8, s27, 0xfffffff
	s_lshr_b32 s9, s8, 2
	s_lshl_b32 s9, s9, 11
	s_add_u32 s9, s9, s100
	s_lshr_b32 s10, s9, 9
	s_mul_i32 s10, s10, 0x2493
	s_lshr_b32 s10, s10, 16
	s_mul_i32 s32, s10, 0xe00
	s_sub_u32 s9, s9, s32
	s_and_b32 s8, s8, 3
	s_cmp_ge_u32 s10, 16
	s_cbranch_scc1 .Lcn_dn_lfCd
	s_lshr_b32 s32, s9, 5
	s_mul_i32 s32, s32, 0x2493
	s_lshr_b32 s32, s32, 16
	s_mul_i32 s33, s32, 0xe0
	s_sub_u32 s33, s9, s33
	s_lshl_b32 s32, s32, 2
	s_add_u32 s32, s32, s8
	s_lshr_b32 s9, s10, 1
	s_and_b32 s10, s10, 1
	s_mul_i32 s8, s9, 0x1c00000
	s_add_u32 s8, s8, 0x4a000000
	s_lshr_b32 s9, s33, 2
	s_lshl_b32 s9, s9, 8
	s_lshl_b32 s10, s10, 7
	s_add_u32 s9, s9, s10
	s_and_b32 s10, s33, 3
	s_lshl_b32 s10, s10, 5
	s_add_u32 s9, s9, s10
	s_lshl_b32 s9, s9, 11
	s_add_u32 s8, s8, s9
	s_lshl_b32 s9, s32, 5
	s_add_u32 s8, s8, s9
	v_readlane_b32 s32, v255, 52
	v_readlane_b32 s33, v255, 53
	s_add_u32 s32, s32, s8
	s_addc_u32 s33, s33, 0
	s_movk_i32 s10, 0x800
	s_mov_b32 s9, 0x42000000
	s_branch .Lcn_dd_lfCd

; __device__ __forceinline__ unsigned pk4_fp8(float a, float b, float c, float d) { int p = __builtin_amdgcn_cvt_pk_fp8_f32(a, b, 0, false); p = __builtin_amdgcn_cvt_pk_fp8_f32(c, d, p, true); return (unsigned)p; }
; __device__ __forceinline__ void witem_store(const WItem& w, const f32x4 (&v)[16]) {
;     if (!w.valid) return;
;     if (w.f8) {
; #pragma unroll
;         for (int j = 0; j < 4; ++j) { u32x4 o; const float sc = w.scale;
;             o.x = pk4_fp8(v[0][j] * sc, v[1][j] * sc, v[2][j] * sc, v[3][j] * sc); o.y = pk4_fp8(v[4][j] * sc, v[5][j] * sc, v[6][j] * sc, v[7][j] * sc);
;             o.z = pk4_fp8(v[8][j] * sc, v[9][j] * sc, v[10][j] * sc, v[11][j] * sc); o.w = pk4_fp8(v[12][j] * sc, v[13][j] * sc, v[14][j] * sc, v[15][j] * sc);
;             *(u32x4*)(w.dst + (size_t)witem_row(w.kind, w.n + j) * w.K + w.k0) = o; }
; __device__ __forceinline__ void p0_weights(const Args& a, LAS unsigned char* lds) {
;     ...
;         else if ((r -= I_FD) < 16 * I_MG) { const int up = r / (8 * I_MG); r -= up * 8 * I_MG; const int e = r / I_MG; r -= e * I_MG; W = a.in[up ? I_MWU : I_MWG] + (size_t)e * D * DFE; w.K = D; w.N = DFE;
;             w.dst = a.ws + WS_MGU_T + (size_t)e * 2 * DFE * D * (MOE_FP8 ? 1 : 2); w.kind = 2 + up; w.f8 = MOE_FP8; w.scale = F8_WGU; }
;         else { r -= 16 * I_MG; const int e = r / I_MD; r -= e * I_MD; W = a.in[I_MWD] + (size_t)e * DFE * D; w.K = DFE; w.N = D; w.dst = a.ws + WS_MD_T + (size_t)e * D * DFE * (MOE_FP8 ? 1 : 2); w.f8 = MOE_FP8; w.scale = F8_WD; }
;         const int nblk = (w.N + 31) >> 5, kb = r / nblk, nb = r - kb * nblk;
;         w.k0 = 128 * kb + 16 * (lane >> 3); w.n = 32 * nb + 4 * (lane & 7); w.valid = w.n < w.N; w.src = W + (size_t)w.k0 * w.N + w.n;
.Lcn_dd_lfCd:
	s_mov_b32 s27, 0
	v_mul_f32_e32 v132, s9, v132
	v_mul_f32_e32 v133, s9, v133
	v_mul_f32_e32 v134, s9, v134
	v_mul_f32_e32 v135, s9, v135
	v_mul_f32_e32 v136, s9, v136
	v_mul_f32_e32 v137, s9, v137
	v_mul_f32_e32 v138, s9, v138
	v_mul_f32_e32 v139, s9, v139
	v_mul_f32_e32 v140, s9, v140
	v_mul_f32_e32 v141, s9, v141
	v_mul_f32_e32 v142, s9, v142
	v_mul_f32_e32 v143, s9, v143
	v_mul_f32_e32 v144, s9, v144
	v_mul_f32_e32 v145, s9, v145
	v_mul_f32_e32 v146, s9, v146
	v_mul_f32_e32 v147, s9, v147
	v_cvt_pk_fp8_f32 v132, v132, v136
	v_cvt_pk_fp8_f32 v133, v133, v137
	v_cvt_pk_fp8_f32 v134, v134, v138
	v_cvt_pk_fp8_f32 v135, v135, v139
	v_cvt_pk_fp8_f32 v132, v140, v144 op_sel:[0,0,1]
	v_cvt_pk_fp8_f32 v133, v141, v145 op_sel:[0,0,1]
	v_cvt_pk_fp8_f32 v134, v142, v146 op_sel:[0,0,1]
	v_cvt_pk_fp8_f32 v135, v143, v147 op_sel:[0,0,1]
	v_and_b32_e32 v136, 63, v0
	v_and_b32_e32 v138, 7, v136
	v_lshrrev_b32_e32 v136, 3, v136
	v_lshlrev_b32_e32 v136, 2, v136
	v_lshlrev_b32_e32 v137, 4, v138
	v_lshlrev_b32_e32 v138, 2, v138
	v_mad_u32_u24 v137, v138, s10, v136
	global_store_dword v137, v132, s[32:33] nt
	v_add_u32_e32 v136, s10, v137
	global_store_dword v136, v133, s[32:33] nt
	v_add_u32_e32 v138, s10, v136
	global_store_dword v138, v134, s[32:33] nt
	v_add_u32_e32 v139, s10, v138
	global_store_dword v139, v135, s[32:33] nt
.Lcn_snone_lfC:
	s_bitcmp1_b32 s28, 31
	s_cbranch_scc0 .Lcn_snone_lfD
	s_and_b32 s8, s28, 0xfffffff
	s_lshr_b32 s9, s8, 2
	s_lshl_b32 s9, s9, 11
	s_add_u32 s9, s9, s100
	s_lshr_b32 s10, s9, 9
	s_mul_i32 s10, s10, 0x2493
	s_lshr_b32 s10, s10, 16
	s_mul_i32 s32, s10, 0xe00
	s_sub_u32 s9, s9, s32
	s_and_b32 s8, s8, 3
	s_cmp_ge_u32 s10, 16
	s_cbranch_scc1 .Lcn_dn_lfDd
	s_lshr_b32 s32, s9, 5
	s_mul_i32 s32, s32, 0x2493
	s_lshr_b32 s32, s32, 16
	s_mul_i32 s33, s32, 0xe0
	s_sub_u32 s33, s9, s33
	s_lshl_b32 s32, s32, 2
	s_add_u32 s32, s32, s8
	s_lshr_b32 s9, s10, 1
	s_and_b32 s10, s10, 1
	s_mul_i32 s8, s9, 0x1c00000
	s_add_u32 s8, s8, 0x4a000000
	s_lshr_b32 s9, s33, 2
	s_lshl_b32 s9, s9, 8
	s_lshl_b32 s10, s10, 7
	s_add_u32 s9, s9, s10
	s_and_b32 s10, s33, 3
	s_lshl_b32 s10, s10, 5
	s_add_u32 s9, s9, s10
	s_lshl_b32 s9, s9, 11
	s_add_u32 s8, s8, s9
	s_lshl_b32 s9, s32, 5
	s_add_u32 s8, s8, s9
	v_readlane_b32 s32, v255, 52
	v_readlane_b32 s33, v255, 53
	s_add_u32 s32, s32, s8
	s_addc_u32 s33, s33, 0
	s_movk_i32 s10, 0x800
	s_mov_b32 s9, 0x42000000
	s_branch .Lcn_dd_lfDd

; __device__ __forceinline__ unsigned pk4_fp8(float a, float b, float c, float d) { int p = __builtin_amdgcn_cvt_pk_fp8_f32(a, b, 0, false); p = __builtin_amdgcn_cvt_pk_fp8_f32(c, d, p, true); return (unsigned)p; }
; __device__ __forceinline__ void witem_store(const WItem& w, const f32x4 (&v)[16]) {
;     if (!w.valid) return;
;     if (w.f8) {
; #pragma unroll
;         for (int j = 0; j < 4; ++j) { u32x4 o; const float sc = w.scale;
;             o.x = pk4_fp8(v[0][j] * sc, v[1][j] * sc, v[2][j] * sc, v[3][j] * sc); o.y = pk4_fp8(v[4][j] * sc, v[5][j] * sc, v[6][j] * sc, v[7][j] * sc);
;             o.z = pk4_fp8(v[8][j] * sc, v[9][j] * sc, v[10][j] * sc, v[11][j] * sc); o.w = pk4_fp8(v[12][j] * sc, v[13][j] * sc, v[14][j] * sc, v[15][j] * sc);
;             *(u32x4*)(w.dst + (size_t)witem_row(w.kind, w.n + j) * w.K + w.k0) = o; }
.Lcn_dd_lfDd:
	s_mov_b32 s28, 0
	v_mul_f32_e32 v148, s9, v148
	v_mul_f32_e32 v149, s9, v149
	v_mul_f32_e32 v150, s9, v150
	v_mul_f32_e32 v151, s9, v151
	v_mul_f32_e32 v152, s9, v152
	v_mul_f32_e32 v153, s9, v153
	v_mul_f32_e32 v154, s9, v154
	v_mul_f32_e32 v155, s9, v155
	v_mul_f32_e32 v156, s9, v156
	v_mul_f32_e32 v157, s9, v157
	v_mul_f32_e32 v158, s9, v158
	v_mul_f32_e32 v159, s9, v159
	v_mul_f32_e32 v160, s9, v160
	v_mul_f32_e32 v161, s9, v161
	v_mul_f32_e32 v162, s9, v162
	v_mul_f32_e32 v163, s9, v163
	v_cvt_pk_fp8_f32 v148, v148, v152
	v_cvt_pk_fp8_f32 v149, v149, v153
	v_cvt_pk_fp8_f32 v150, v150, v154
	v_cvt_pk_fp8_f32 v151, v151, v155
	v_cvt_pk_fp8_f32 v148, v156, v160 op_sel:[0,0,1]
	v_cvt_pk_fp8_f32 v149, v157, v161 op_sel:[0,0,1]
	v_cvt_pk_fp8_f32 v150, v158, v162 op_sel:[0,0,1]
	v_cvt_pk_fp8_f32 v151, v159, v163 op_sel:[0,0,1]
	v_and_b32_e32 v152, 63, v0
	v_and_b32_e32 v154, 7, v152
	v_lshrrev_b32_e32 v152, 3, v152
	v_lshlrev_b32_e32 v152, 2, v152
	v_lshlrev_b32_e32 v153, 4, v154
	v_lshlrev_b32_e32 v154, 2, v154
	v_mad_u32_u24 v153, v154, s10, v152
	global_store_dword v153, v148, s[32:33] nt
	v_add_u32_e32 v152, s10, v153
	global_store_dword v152, v149, s[32:33] nt
	v_add_u32_e32 v154, s10, v152
	global_store_dword v154, v150, s[32:33] nt
	v_add_u32_e32 v155, s10, v154
	global_store_dword v155, v151, s[32:33] nt
